# conv-in-NSA: fp8 bytes of four k-consecutive items gathered in the wave's idle top-k LDS slab and written as whole 128-byte lines (4x fewer store requests); one register set, no load issue at the last
# speedup vs baseline: 1.0364x; 1.0149x over previous
; __device__ __forceinline__ void p0_weights(const Args& a, LAS unsigned char* lds) {
;     ...
;         else if ((r -= I_FD) < 16 * I_MG) { const int up = r / (8 * I_MG); r -= up * 8 * I_MG; const int e = r / I_MG; r -= e * I_MG; W = a.in[up ? I_MWU : I_MWG] + (size_t)e * D * DFE; w.K = D; w.N = DFE;
;             w.dst = a.ws + WS_MGU_T + (size_t)e * 2 * DFE * D * (MOE_FP8 ? 1 : 2); w.kind = 2 + up; w.f8 = MOE_FP8; w.scale = F8_WGU; }
;         else { r -= 16 * I_MG; const int e = r / I_MD; r -= e * I_MD; W = a.in[I_MWD] + (size_t)e * DFE * D; w.K = DFE; w.N = D; w.dst = a.ws + WS_MD_T + (size_t)e * D * DFE * (MOE_FP8 ? 1 : 2); w.f8 = MOE_FP8; w.scale = F8_WD; }
;         const int nblk = (w.N + 31) >> 5, kb = r / nblk, nb = r - kb * nblk;
;         w.k0 = 128 * kb + 16 * (lane >> 3); w.n = 32 * nb + 4 * (lane & 7); w.valid = w.n < w.N; w.src = W + (size_t)w.k0 * w.N + w.n;
; __device__ __forceinline__ void nsa_unit(const Args& a, LAS unsigned char* lds, int b, int kvh, int qb) {
;     ...
; #pragma unroll
;     for (int dt = 0; dt < 4; ++dt)
; #pragma unroll
;         for (int i = 0; i < 16; ++i) o[dt][i] = 0.f;
;     float mrun = -1e30f, lrun = 0.f;
;     f32x16 p0, p1;
; #pragma unroll
;     for (int i = 0; i < 16; ++i) { p0[i] = 0.f; p1[i] = 0.f; }
;     bf16x8 pf[2][2];
;     if (w >= 4) asm volatile("s_barrier" ::: "memory");
.LBB0_894:
	s_cmp_lt_i32 s15, -1
	s_cbranch_scc1 .LBB0_919
	v_mov_b32_e32 v49, v47
	s_lshl_b32 s0, s72, 1
	s_max_i32 s1, s72, 8
	v_mov_b32_e32 v60, v47
	v_mov_b32_e32 v61, v47
	v_lshl_add_u64 v[206:207], s[30:31], 0, v[48:49]
	s_sub_i32 s63, s0, s1
	v_mov_b32_e32 v46, v47
	v_mov_b32_e32 v48, v47
	v_mov_b32_e32 v50, v47
	v_mov_b32_e32 v51, v47
	v_mov_b32_e32 v52, v47
	v_mov_b32_e32 v53, v47
	v_mov_b32_e32 v54, v47
	v_mov_b32_e32 v55, v47
	v_mov_b32_e32 v56, v47
	v_mov_b32_e32 v57, v47
	v_mov_b32_e32 v58, v47
	v_mov_b32_e32 v59, v47
	v_mov_b64_e32 v[108:109], v[60:61]
	v_mov_b64_e32 v[124:125], v[60:61]
	v_mov_b64_e32 v[140:141], v[60:61]
	v_mov_b64_e32 v[156:157], v[60:61]
	v_mov_b64_e32 v[76:77], v[60:61]
	v_mov_b64_e32 v[92:93], v[60:61]
	v_add_u32_e32 v43, 1, v249
	s_add_i32 s23, s63, 11
	s_add_i32 s24, s63, 10
	s_mov_b32 s62, 2
	s_add_i32 s63, s63, 2
	s_mov_b32 s74, 0
	v_mov_b32_e32 v208, 0xf149f2ca
	v_mov_b32_e32 v209, 0
	s_movk_i32 s75, 0xc000
	v_mov_b64_e32 v[106:107], v[58:59]
	v_mov_b64_e32 v[104:105], v[56:57]
	v_mov_b64_e32 v[102:103], v[54:55]
	v_mov_b64_e32 v[100:101], v[52:53]
	v_mov_b64_e32 v[98:99], v[50:51]
	v_mov_b64_e32 v[96:97], v[48:49]
	v_mov_b64_e32 v[94:95], v[46:47]
	v_mov_b64_e32 v[122:123], v[58:59]
	v_mov_b64_e32 v[120:121], v[56:57]
	v_mov_b64_e32 v[118:119], v[54:55]
	v_mov_b64_e32 v[116:117], v[52:53]
	v_mov_b64_e32 v[114:115], v[50:51]
	v_mov_b64_e32 v[112:113], v[48:49]
	v_mov_b64_e32 v[110:111], v[46:47]
	v_mov_b64_e32 v[138:139], v[58:59]
	v_mov_b64_e32 v[136:137], v[56:57]
	v_mov_b64_e32 v[134:135], v[54:55]
	v_mov_b64_e32 v[132:133], v[52:53]
	v_mov_b64_e32 v[130:131], v[50:51]
	v_mov_b64_e32 v[128:129], v[48:49]
	v_mov_b64_e32 v[126:127], v[46:47]
	v_mov_b64_e32 v[154:155], v[58:59]
	v_mov_b64_e32 v[152:153], v[56:57]
	v_mov_b64_e32 v[150:151], v[54:55]
	v_mov_b64_e32 v[148:149], v[52:53]
	v_mov_b64_e32 v[146:147], v[50:51]
	v_mov_b64_e32 v[144:145], v[48:49]
	v_mov_b64_e32 v[142:143], v[46:47]
	v_mov_b64_e32 v[74:75], v[58:59]
	v_mov_b64_e32 v[72:73], v[56:57]
	v_mov_b64_e32 v[70:71], v[54:55]
	v_mov_b64_e32 v[68:69], v[52:53]
	v_mov_b64_e32 v[66:67], v[50:51]
	v_mov_b64_e32 v[64:65], v[48:49]
	v_mov_b64_e32 v[62:63], v[46:47]
	v_mov_b64_e32 v[90:91], v[58:59]
	v_mov_b64_e32 v[88:89], v[56:57]
	v_mov_b64_e32 v[86:87], v[54:55]
	v_mov_b64_e32 v[84:85], v[52:53]
	v_mov_b64_e32 v[82:83], v[50:51]
	v_mov_b64_e32 v[80:81], v[48:49]
	v_mov_b64_e32 v[78:79], v[46:47]
	s_mov_b32 s67, 0
	s_and_b32 s12, s101, 3
	s_lshl_b32 s12, s12, 28
	s_andn2_b32 s101, s101, 0x30000000
	s_or_b32 s101, s101, s12
	s_and_b32 s12, s101, 0xfffffff
	s_cmp_ge_u32 s12, 168
	s_cbranch_scc1 .Lcn_ldum_n0s
	s_and_b32 s12, s101, 0xfffffff
	s_lshr_b32 s13, s12, 2
	s_lshl_b32 s13, s13, 11
	s_add_u32 s13, s13, s100
	s_lshr_b32 s65, s13, 9
	s_mul_i32 s65, s65, 0x2493
	s_lshr_b32 s65, s65, 16
	s_mul_i32 s66, s65, 0xe00
	s_sub_u32 s13, s13, s66
	s_and_b32 s12, s12, 3
	s_cmp_ge_u32 s65, 16
	s_cbranch_scc1 .Lcn_dn_n0ss
	s_lshr_b32 s66, s13, 5
	s_mul_i32 s66, s66, 0x2493
	s_lshr_b32 s66, s66, 16
	s_mul_i32 s0, s66, 0xe0
	s_sub_u32 s0, s13, s0
	s_lshl_b32 s66, s66, 2
	s_add_u32 s66, s66, s12
	s_lshr_b32 s13, s65, 1
	s_and_b32 s65, s65, 1
	s_mul_i32 s12, s13, 0x3800000
	s_mul_i32 s13, s66, 0xe0000
	s_add_u32 s12, s12, s13
	s_lshl_b32 s13, s0, 7
	s_add_u32 s12, s12, s13
	v_readlane_b32 s32, v255, 46
	v_readlane_b32 s33, v255, 47
	s_cmp_eq_u32 s65, 0
	s_cselect_b32 s32, s98, s32
	s_cselect_b32 s33, s99, s33
	s_add_u32 s32, s32, s12
	s_addc_u32 s33, s33, 0
	s_movk_i32 s1, 0x7000
	s_branch .Lcn_dd_n0ss
.Lcn_dn_n0ss:
	s_lshr_b32 s66, s13, 6
	s_and_b32 s0, s13, 63
	s_lshl_b32 s66, s66, 2
	s_add_u32 s66, s66, s12
	s_sub_u32 s13, s65, 16
	s_mul_i32 s12, s13, 0x3800000
	s_lshl_b32 s13, s66, 18
	s_add_u32 s12, s12, s13
	s_lshl_b32 s13, s0, 7
	s_add_u32 s12, s12, s13
	v_readlane_b32 s32, v255, 48
	v_readlane_b32 s33, v255, 49
	s_add_u32 s32, s32, s12
	s_addc_u32 s33, s33, 0
	s_movk_i32 s1, 0x2000
.Lcn_dd_n0ss:
	s_and_b32 s25, s101, 0xfffffff
	s_bitset1_b32 s25, 31
	s_add_u32 s101, s101, 1
	s_branch .Lcn_lgo_n0s

; __device__ __forceinline__ void witem_load(const WItem& w, f32x4 (&v)[16]) {
;     if (!w.valid) return;
; #pragma unroll
;     for (int i = 0; i < 16; ++i) v[i] = *(const f32x4*)(w.src + (size_t)i * w.N);
; }
.Lcn_lgo_n0s:
	v_and_b32_e32 v224, 63, v0
	v_and_b32_e32 v253, 7, v224
	v_lshrrev_b32_e32 v224, 3, v224
	v_lshlrev_b32_e32 v224, 2, v224
	v_lshlrev_b32_e32 v225, 4, v253
	v_lshlrev_b32_e32 v253, 2, v253
	v_mad_u32_u24 v254, v224, s1, v225
	global_load_dwordx4 v[212:215], v254, s[32:33] nt
	s_add_u32 s32, s32, s1
	s_addc_u32 s33, s33, 0
	global_load_dwordx4 v[216:219], v254, s[32:33] nt
	s_add_u32 s32, s32, s1
	s_addc_u32 s33, s33, 0
	global_load_dwordx4 v[220:223], v254, s[32:33] nt
	s_add_u32 s32, s32, s1
	s_addc_u32 s33, s33, 0
	global_load_dwordx2 v[224:225], v254, s[32:33] offset:0 nt
	global_load_dword v253, v254, s[32:33] offset:8 nt
	global_load_dword v254, v254, s[32:33] offset:12 nt
	s_branch .LBB0_897

; __device__ __forceinline__ unsigned pk4_fp8(float a, float b, float c, float d) { int p = __builtin_amdgcn_cvt_pk_fp8_f32(a, b, 0, false); p = __builtin_amdgcn_cvt_pk_fp8_f32(c, d, p, true); return (unsigned)p; }
; __device__ __forceinline__ void witem_store(const WItem& w, const f32x4 (&v)[16]) {
;     if (!w.valid) return;
;     if (w.f8) {
; #pragma unroll
;         for (int j = 0; j < 4; ++j) { u32x4 o; const float sc = w.scale;
;             o.x = pk4_fp8(v[0][j] * sc, v[1][j] * sc, v[2][j] * sc, v[3][j] * sc); o.y = pk4_fp8(v[4][j] * sc, v[5][j] * sc, v[6][j] * sc, v[7][j] * sc);
;             o.z = pk4_fp8(v[8][j] * sc, v[9][j] * sc, v[10][j] * sc, v[11][j] * sc); o.w = pk4_fp8(v[12][j] * sc, v[13][j] * sc, v[14][j] * sc, v[15][j] * sc);
;             *(u32x4*)(w.dst + (size_t)witem_row(w.kind, w.n + j) * w.K + w.k0) = o; }
; __device__ __forceinline__ void p0_weights(const Args& a, LAS unsigned char* lds) {
;     ...
;         else if ((r -= I_FD) < 16 * I_MG) { const int up = r / (8 * I_MG); r -= up * 8 * I_MG; const int e = r / I_MG; r -= e * I_MG; W = a.in[up ? I_MWU : I_MWG] + (size_t)e * D * DFE; w.K = D; w.N = DFE;
;             w.dst = a.ws + WS_MGU_T + (size_t)e * 2 * DFE * D * (MOE_FP8 ? 1 : 2); w.kind = 2 + up; w.f8 = MOE_FP8; w.scale = F8_WGU; }
;         else { r -= 16 * I_MG; const int e = r / I_MD; r -= e * I_MD; W = a.in[I_MWD] + (size_t)e * DFE * D; w.K = DFE; w.N = D; w.dst = a.ws + WS_MD_T + (size_t)e * D * DFE * (MOE_FP8 ? 1 : 2); w.f8 = MOE_FP8; w.scale = F8_WD; }
;         const int nblk = (w.N + 31) >> 5, kb = r / nblk, nb = r - kb * nblk;
;         w.k0 = 128 * kb + 16 * (lane >> 3); w.n = 32 * nb + 4 * (lane & 7); w.valid = w.n < w.N; w.src = W + (size_t)w.k0 * w.N + w.n;
.Lcn_wd_n0:
	s_bitcmp1_b32 s25, 31
	s_cbranch_scc0 .Lcn_snone_n0l
	s_and_b32 s12, s25, 0xfffffff
	s_lshr_b32 s13, s12, 2
	s_lshl_b32 s13, s13, 11
	s_add_u32 s13, s13, s100
	s_lshr_b32 s65, s13, 9
	s_mul_i32 s65, s65, 0x2493
	s_lshr_b32 s65, s65, 16
	s_mul_i32 s66, s65, 0xe00
	s_sub_u32 s13, s13, s66
	s_and_b32 s12, s12, 3
	s_cmp_ge_u32 s65, 16
	s_cbranch_scc1 .Lcn_dn_n0ld
	s_lshr_b32 s66, s13, 5
	s_mul_i32 s66, s66, 0x2493
	s_lshr_b32 s66, s66, 16
	s_mul_i32 s0, s66, 0xe0
	s_sub_u32 s0, s13, s0
	s_lshl_b32 s66, s66, 2
	s_add_u32 s66, s66, s12
	s_lshr_b32 s13, s65, 1
	s_and_b32 s65, s65, 1
	s_mul_i32 s12, s13, 0x1c00000
	s_add_u32 s12, s12, 0x4a000000
	s_lshr_b32 s13, s0, 2
	s_lshl_b32 s13, s13, 8
	s_lshl_b32 s65, s65, 7
	s_add_u32 s13, s13, s65
	s_and_b32 s65, s0, 3
	s_lshl_b32 s65, s65, 5
	s_add_u32 s13, s13, s65
	s_lshl_b32 s13, s13, 11
	s_add_u32 s12, s12, s13
	s_lshl_b32 s13, s66, 5
	s_add_u32 s12, s12, s13
	v_readlane_b32 s32, v255, 52
	v_readlane_b32 s33, v255, 53
	s_add_u32 s32, s32, s12
	s_addc_u32 s33, s33, 0
	s_movk_i32 s1, 0x800
	s_mov_b32 s0, 0x42000000
	s_branch .Lcn_dd_n0ld
.Lcn_dn_n0ld:
	s_lshr_b32 s66, s13, 6
	s_and_b32 s0, s13, 63
	s_lshl_b32 s66, s66, 2
	s_add_u32 s66, s66, s12
	s_sub_u32 s13, s65, 16
	s_mul_i32 s12, s13, 0xe00000
	s_add_u32 s12, s12, 0x66000000
	s_mul_i32 s13, s0, 0x38000
	s_add_u32 s12, s12, s13
	s_lshl_b32 s13, s66, 5
	s_add_u32 s12, s12, s13
	v_readlane_b32 s32, v255, 52
	v_readlane_b32 s33, v255, 53
	s_add_u32 s32, s32, s12
	s_addc_u32 s33, s33, 0
	s_movk_i32 s1, 0x1c00
	s_mov_b32 s0, 0x43000000
.Lcn_dd_n0ld:
	v_mul_f32_e32 v212, s0, v212
	v_mul_f32_e32 v213, s0, v213
	v_mul_f32_e32 v214, s0, v214
	v_mul_f32_e32 v215, s0, v215
	v_mul_f32_e32 v216, s0, v216
	v_mul_f32_e32 v217, s0, v217
	v_mul_f32_e32 v218, s0, v218
	v_mul_f32_e32 v219, s0, v219
	v_mul_f32_e32 v220, s0, v220
	v_mul_f32_e32 v221, s0, v221
	v_mul_f32_e32 v222, s0, v222
	v_mul_f32_e32 v223, s0, v223
	v_mul_f32_e32 v224, s0, v224
	v_mul_f32_e32 v225, s0, v225
	v_mul_f32_e32 v253, s0, v253
	v_mul_f32_e32 v254, s0, v254
	v_cvt_pk_fp8_f32 v212, v212, v216
	v_cvt_pk_fp8_f32 v213, v213, v217
	v_cvt_pk_fp8_f32 v214, v214, v218
	v_cvt_pk_fp8_f32 v215, v215, v219
	v_cvt_pk_fp8_f32 v212, v220, v224 op_sel:[0,0,1]
	v_cvt_pk_fp8_f32 v213, v221, v225 op_sel:[0,0,1]
	v_cvt_pk_fp8_f32 v214, v222, v253 op_sel:[0,0,1]
	v_cvt_pk_fp8_f32 v215, v223, v254 op_sel:[0,0,1]
	s_and_b32 s12, s25, 3
	v_and_b32_e32 v216, 63, v0
	v_and_b32_e32 v217, 7, v216
	v_lshrrev_b32_e32 v216, 3, v216
	v_and_b32_e32 v218, 3, v217
	v_xor_b32_e32 v218, s12, v218
	v_lshlrev_b32_e32 v218, 5, v218
	v_lshl_add_u32 v218, v216, 2, v218
	v_lshl_add_u32 v218, v217, 9, v218
	v_and_b32_e32 v219, 0x1c0, v0
	v_lshl_add_u32 v218, v219, 6, v218
	v_add_u32_e32 v218, 0x1c000, v218
	ds_write_b32 v218, v212 offset:0
	ds_write_b32 v218, v213 offset:128
	ds_write_b32 v218, v214 offset:256
	ds_write_b32 v218, v215 offset:384
	s_mov_b32 s67, s25
	s_mov_b32 s25, 0
.Lcn_snone_n0l:
	s_and_b32 s12, s67, 0x80000003
	s_cmp_eq_u32 s12, 0x80000003
	s_cbranch_scc0 .Lcn_fnone_n0l
	s_bitcmp1_b32 s67, 31
	s_cbranch_scc0 .Lcn_fnone_n0l
	s_and_b32 s12, s67, 0xfffffff
	s_lshr_b32 s13, s12, 2
	s_lshl_b32 s13, s13, 11
	s_add_u32 s13, s13, s100
	s_lshr_b32 s65, s13, 9
	s_mul_i32 s65, s65, 0x2493
	s_lshr_b32 s65, s65, 16
	s_mul_i32 s66, s65, 0xe00
	s_sub_u32 s13, s13, s66
	s_mov_b32 s12, 0
	s_cmp_ge_u32 s65, 16
	s_cbranch_scc1 .Lcn_dn_n0lf
	s_lshr_b32 s66, s13, 5
	s_mul_i32 s66, s66, 0x2493
	s_lshr_b32 s66, s66, 16
	s_mul_i32 s0, s66, 0xe0
	s_sub_u32 s0, s13, s0
	s_lshl_b32 s66, s66, 2
	s_add_u32 s66, s66, s12
	s_lshr_b32 s13, s65, 1
	s_and_b32 s65, s65, 1
	s_mul_i32 s12, s13, 0x1c00000
	s_add_u32 s12, s12, 0x4a000000
	s_lshr_b32 s13, s0, 2
	s_lshl_b32 s13, s13, 8
	s_lshl_b32 s65, s65, 7
	s_add_u32 s13, s13, s65
	s_and_b32 s65, s0, 3
	s_lshl_b32 s65, s65, 5
	s_add_u32 s13, s13, s65
	s_lshl_b32 s13, s13, 11
	s_add_u32 s12, s12, s13
	s_lshl_b32 s13, s66, 5
	s_add_u32 s12, s12, s13
	v_readlane_b32 s32, v255, 52
	v_readlane_b32 s33, v255, 53
	s_add_u32 s32, s32, s12
	s_addc_u32 s33, s33, 0
	s_movk_i32 s1, 0x800
	s_mov_b32 s0, 0x42000000
	s_branch .Lcn_dd_n0lf

; __device__ __forceinline__ unsigned pk4_fp8(float a, float b, float c, float d) { int p = __builtin_amdgcn_cvt_pk_fp8_f32(a, b, 0, false); p = __builtin_amdgcn_cvt_pk_fp8_f32(c, d, p, true); return (unsigned)p; }
; __device__ __forceinline__ void witem_store(const WItem& w, const f32x4 (&v)[16]) {
;     if (!w.valid) return;
;     if (w.f8) {
; #pragma unroll
;         for (int j = 0; j < 4; ++j) { u32x4 o; const float sc = w.scale;
;             o.x = pk4_fp8(v[0][j] * sc, v[1][j] * sc, v[2][j] * sc, v[3][j] * sc); o.y = pk4_fp8(v[4][j] * sc, v[5][j] * sc, v[6][j] * sc, v[7][j] * sc);
;             o.z = pk4_fp8(v[8][j] * sc, v[9][j] * sc, v[10][j] * sc, v[11][j] * sc); o.w = pk4_fp8(v[12][j] * sc, v[13][j] * sc, v[14][j] * sc, v[15][j] * sc);
;             *(u32x4*)(w.dst + (size_t)witem_row(w.kind, w.n + j) * w.K + w.k0) = o; }
; __device__ __forceinline__ void p0_weights(const Args& a, LAS unsigned char* lds) {
;     ...
;     { f32x4 v[16], vn[16];
;       WItem cur = decode(gw); witem_load(cur, v);
; #pragma unroll 1
;       for (int it = gw; it < NIT; it += NGW) {
;           const WItem nxt = decode(it + NGW); witem_load(nxt, vn);
;           __builtin_amdgcn_sched_barrier(0);
;           witem_store(cur, v);
;           __builtin_amdgcn_sched_barrier(0);
; #pragma unroll
;           for (int i = 0; i < 16; ++i) v[i] = vn[i];
;           cur = nxt; } }
.Lcn_dd_n0lf:
	s_lshr_b32 s12, s101, 28
	s_and_b32 s12, s12, 3
	s_and_b32 s13, s67, 3
	s_add_u32 s13, s13, 1
	s_sub_u32 s13, s13, s12
	v_and_b32_e32 v224, 63, v0
	v_lshrrev_b32_e32 v225, 3, v224
	v_and_b32_e32 v224, 7, v224
	v_lshrrev_b32_e32 v253, 1, v224
	v_subrev_u32_e32 v254, s12, v253
	v_cmp_gt_u32_e32 vcc, s13, v254
	v_lshrrev_b32_e32 v254, 2, v225
	v_xor_b32_e32 v254, v254, v253
	v_lshlrev_b32_e32 v254, 1, v254
	v_and_b32_e32 v253, 1, v224
	v_or_b32_e32 v254, v254, v253
	v_lshlrev_b32_e32 v254, 4, v254
	v_lshl_add_u32 v254, v225, 7, v254
	v_and_b32_e32 v253, 0x1c0, v0
	v_lshl_add_u32 v254, v253, 6, v254
	v_add_u32_e32 v254, 0x1c000, v254
	v_xor_b32_e32 v253, 64, v254
	v_mul_u32_u24_e32 v225, s1, v225
	v_lshl_add_u32 v225, v224, 4, v225
	s_and_saveexec_b64 s[12:13], vcc
	ds_read_b128 v[212:215], v254
	ds_read_b128 v[216:219], v253 offset:1024
	ds_read_b128 v[220:223], v254 offset:2048
	s_lshl_b32 s1, s1, 3
	s_waitcnt lgkmcnt(0)
	global_store_dwordx4 v225, v[212:215], s[32:33] nt
	s_add_u32 s32, s32, s1
	s_addc_u32 s33, s33, 0
	s_nop 1
	ds_read_b128 v[212:215], v253 offset:3072
	global_store_dwordx4 v225, v[216:219], s[32:33] nt
	s_add_u32 s32, s32, s1
	s_addc_u32 s33, s33, 0
	global_store_dwordx4 v225, v[220:223], s[32:33] nt
	s_add_u32 s32, s32, s1
	s_addc_u32 s33, s33, 0
	s_waitcnt lgkmcnt(0)
	global_store_dwordx4 v225, v[212:215], s[32:33] nt
	s_mov_b64 exec, s[12:13]
	s_and_b32 s65, s67, 3
	s_add_u32 s65, s65, 1
	s_and_b32 s65, s65, 3
	s_lshl_b32 s65, s65, 28
	s_andn2_b32 s101, s101, 0x30000000
	s_or_b32 s101, s101, s65
	s_mov_b32 s67, 0
.Lcn_fnone_n0l:
	s_mov_b32 s25, 0
	s_cmp_gt_i32 s74, s15
	s_cbranch_scc1 .Lcn_lskip_n0l
	s_and_b32 s12, s101, 0xfffffff
	s_cmp_ge_u32 s12, 168
	s_cbranch_scc1 .Lcn_ldum_n0l
	s_and_b32 s12, s101, 0xfffffff
	s_lshr_b32 s13, s12, 2
	s_lshl_b32 s13, s13, 11
	s_add_u32 s13, s13, s100
	s_lshr_b32 s65, s13, 9
	s_mul_i32 s65, s65, 0x2493
	s_lshr_b32 s65, s65, 16
	s_mul_i32 s66, s65, 0xe00
	s_sub_u32 s13, s13, s66
	s_and_b32 s12, s12, 3
	s_cmp_ge_u32 s65, 16
	s_cbranch_scc1 .Lcn_dn_n0ls
	s_lshr_b32 s66, s13, 5
	s_mul_i32 s66, s66, 0x2493
	s_lshr_b32 s66, s66, 16
	s_mul_i32 s0, s66, 0xe0
	s_sub_u32 s0, s13, s0
	s_lshl_b32 s66, s66, 2
	s_add_u32 s66, s66, s12
	s_lshr_b32 s13, s65, 1
	s_and_b32 s65, s65, 1
	s_mul_i32 s12, s13, 0x3800000
	s_mul_i32 s13, s66, 0xe0000
	s_add_u32 s12, s12, s13
	s_lshl_b32 s13, s0, 7
	s_add_u32 s12, s12, s13
	v_readlane_b32 s32, v255, 46
	v_readlane_b32 s33, v255, 47
	s_cmp_eq_u32 s65, 0
	s_cselect_b32 s32, s98, s32
	s_cselect_b32 s33, s99, s33
	s_add_u32 s32, s32, s12
	s_addc_u32 s33, s33, 0
	s_movk_i32 s1, 0x7000
	s_branch .Lcn_dd_n0ls

; __device__ __forceinline__ void witem_load(const WItem& w, f32x4 (&v)[16]) {
;     if (!w.valid) return;
; #pragma unroll
;     for (int i = 0; i < 16; ++i) v[i] = *(const f32x4*)(w.src + (size_t)i * w.N);
; }
; __device__ __forceinline__ void nsa_unit(const Args& a, LAS unsigned char* lds, int b, int kvh, int qb) {
;     ...
;     for (int it = 0; it <= nTot; ++it) {
;         if (it + 1 < nTot) asm volatile("s_waitcnt vmcnt(4) lgkmcnt(0)\n\ts_barrier" ::: "memory"); else asm volatile("s_waitcnt vmcnt(0) lgkmcnt(0)\n\ts_barrier" ::: "memory");
.Lcn_lgo_n0l:
	v_and_b32_e32 v224, 63, v0
	v_and_b32_e32 v253, 7, v224
	v_lshrrev_b32_e32 v224, 3, v224
	v_lshlrev_b32_e32 v224, 2, v224
	v_lshlrev_b32_e32 v225, 4, v253
	v_lshlrev_b32_e32 v253, 2, v253
	v_mad_u32_u24 v254, v224, s1, v225
	global_load_dwordx4 v[212:215], v254, s[32:33] nt
	s_add_u32 s32, s32, s1
	s_addc_u32 s33, s33, 0
	global_load_dwordx4 v[216:219], v254, s[32:33] nt
	s_add_u32 s32, s32, s1
	s_addc_u32 s33, s33, 0
	global_load_dwordx4 v[220:223], v254, s[32:33] nt
	s_add_u32 s32, s32, s1
	s_addc_u32 s33, s33, 0
	global_load_dwordx2 v[224:225], v254, s[32:33] offset:0 nt
	global_load_dword v253, v254, s[32:33] offset:8 nt
	global_load_dword v254, v254, s[32:33] offset:12 nt
.Lcn_lskip_n0l:
	s_add_i32 s74, s74, 1
	s_addk_i32 s75, 0x4000
	s_add_i32 s62, s62, 1
	s_cmp_eq_u32 s23, s74
	s_cbranch_scc1 .Lcn_exit_n0
.LBB0_897:
	s_cmp_ge_i32 s74, s15
	s_mov_b64 s[0:1], -1
	s_cbranch_scc0 .LBB0_900
	s_waitcnt vmcnt(6) lgkmcnt(0)
	s_barrier
	s_cbranch_execz .LBB0_901

; __device__ __forceinline__ void nsa_unit(const Args& a, LAS unsigned char* lds, int b, int kvh, int qb) {
;     ...
;         asm volatile("s_waitcnt lgkmcnt(0)\n\ts_barrier" ::: "memory");
.LBB0_901:
	s_waitcnt vmcnt(10) lgkmcnt(0)
	s_barrier
	s_cmp_lg_u32 s74, 0
	s_cselect_b64 s[0:1], -1, 0
	s_cmp_eq_u32 s74, 0
	s_cbranch_scc1 .LBB0_912

; __device__ __forceinline__ void p0_weights(const Args& a, LAS unsigned char* lds) {
;     ...
;         else if ((r -= I_FD) < 16 * I_MG) { const int up = r / (8 * I_MG); r -= up * 8 * I_MG; const int e = r / I_MG; r -= e * I_MG; W = a.in[up ? I_MWU : I_MWG] + (size_t)e * D * DFE; w.K = D; w.N = DFE;
;             w.dst = a.ws + WS_MGU_T + (size_t)e * 2 * DFE * D * (MOE_FP8 ? 1 : 2); w.kind = 2 + up; w.f8 = MOE_FP8; w.scale = F8_WGU; }
;         else { r -= 16 * I_MG; const int e = r / I_MD; r -= e * I_MD; W = a.in[I_MWD] + (size_t)e * DFE * D; w.K = DFE; w.N = D; w.dst = a.ws + WS_MD_T + (size_t)e * D * DFE * (MOE_FP8 ? 1 : 2); w.f8 = MOE_FP8; w.scale = F8_WD; }
;         const int nblk = (w.N + 31) >> 5, kb = r / nblk, nb = r - kb * nblk;
;         w.k0 = 128 * kb + 16 * (lane >> 3); w.n = 32 * nb + 4 * (lane & 7); w.valid = w.n < w.N; w.src = W + (size_t)w.k0 * w.N + w.n;
.Lcn_exit_n0:
	s_bitcmp1_b32 s25, 31
	s_cbranch_scc0 .Lcn_xnone_n0
	s_waitcnt vmcnt(0)
	s_bitcmp1_b32 s25, 31
	s_cbranch_scc0 .Lcn_snone_n0x
	s_and_b32 s12, s25, 0xfffffff
	s_lshr_b32 s13, s12, 2
	s_lshl_b32 s13, s13, 11
	s_add_u32 s13, s13, s100
	s_lshr_b32 s65, s13, 9
	s_mul_i32 s65, s65, 0x2493
	s_lshr_b32 s65, s65, 16
	s_mul_i32 s66, s65, 0xe00
	s_sub_u32 s13, s13, s66
	s_and_b32 s12, s12, 3
	s_cmp_ge_u32 s65, 16
	s_cbranch_scc1 .Lcn_dn_n0xd
	s_lshr_b32 s66, s13, 5
	s_mul_i32 s66, s66, 0x2493
	s_lshr_b32 s66, s66, 16
	s_mul_i32 s0, s66, 0xe0
	s_sub_u32 s0, s13, s0
	s_lshl_b32 s66, s66, 2
	s_add_u32 s66, s66, s12
	s_lshr_b32 s13, s65, 1
	s_and_b32 s65, s65, 1
	s_mul_i32 s12, s13, 0x1c00000
	s_add_u32 s12, s12, 0x4a000000
	s_lshr_b32 s13, s0, 2
	s_lshl_b32 s13, s13, 8
	s_lshl_b32 s65, s65, 7
	s_add_u32 s13, s13, s65
	s_and_b32 s65, s0, 3
	s_lshl_b32 s65, s65, 5
	s_add_u32 s13, s13, s65
	s_lshl_b32 s13, s13, 11
	s_add_u32 s12, s12, s13
	s_lshl_b32 s13, s66, 5
	s_add_u32 s12, s12, s13
	v_readlane_b32 s32, v255, 52
	v_readlane_b32 s33, v255, 53
	s_add_u32 s32, s32, s12
	s_addc_u32 s33, s33, 0
	s_movk_i32 s1, 0x800
	s_mov_b32 s0, 0x42000000
	s_branch .Lcn_dd_n0xd

; __device__ __forceinline__ void p0_weights(const Args& a, LAS unsigned char* lds) {
;     ...
;         else if ((r -= I_FD) < 16 * I_MG) { const int up = r / (8 * I_MG); r -= up * 8 * I_MG; const int e = r / I_MG; r -= e * I_MG; W = a.in[up ? I_MWU : I_MWG] + (size_t)e * D * DFE; w.K = D; w.N = DFE;
;             w.dst = a.ws + WS_MGU_T + (size_t)e * 2 * DFE * D * (MOE_FP8 ? 1 : 2); w.kind = 2 + up; w.f8 = MOE_FP8; w.scale = F8_WGU; }
;         else { r -= 16 * I_MG; const int e = r / I_MD; r -= e * I_MD; W = a.in[I_MWD] + (size_t)e * DFE * D; w.K = DFE; w.N = D; w.dst = a.ws + WS_MD_T + (size_t)e * D * DFE * (MOE_FP8 ? 1 : 2); w.f8 = MOE_FP8; w.scale = F8_WD; }
;         const int nblk = (w.N + 31) >> 5, kb = r / nblk, nb = r - kb * nblk;
;         w.k0 = 128 * kb + 16 * (lane >> 3); w.n = 32 * nb + 4 * (lane & 7); w.valid = w.n < w.N; w.src = W + (size_t)w.k0 * w.N + w.n;
.Lcn_snone_n0x:
.Lcn_xnone_n0:
	s_bitcmp1_b32 s67, 31
	s_cbranch_scc0 .Lcn_fnone_n0x
	s_and_b32 s12, s67, 0xfffffff
	s_lshr_b32 s13, s12, 2
	s_lshl_b32 s13, s13, 11
	s_add_u32 s13, s13, s100
	s_lshr_b32 s65, s13, 9
	s_mul_i32 s65, s65, 0x2493
	s_lshr_b32 s65, s65, 16
	s_mul_i32 s66, s65, 0xe00
	s_sub_u32 s13, s13, s66
	s_mov_b32 s12, 0
	s_cmp_ge_u32 s65, 16
	s_cbranch_scc1 .Lcn_dn_n0xf
	s_lshr_b32 s66, s13, 5
	s_mul_i32 s66, s66, 0x2493
	s_lshr_b32 s66, s66, 16
	s_mul_i32 s0, s66, 0xe0
	s_sub_u32 s0, s13, s0
	s_lshl_b32 s66, s66, 2
	s_add_u32 s66, s66, s12
	s_lshr_b32 s13, s65, 1
	s_and_b32 s65, s65, 1
	s_mul_i32 s12, s13, 0x1c00000
	s_add_u32 s12, s12, 0x4a000000
	s_lshr_b32 s13, s0, 2
	s_lshl_b32 s13, s13, 8
	s_lshl_b32 s65, s65, 7
	s_add_u32 s13, s13, s65
	s_and_b32 s65, s0, 3
	s_lshl_b32 s65, s65, 5
	s_add_u32 s13, s13, s65
	s_lshl_b32 s13, s13, 11
	s_add_u32 s12, s12, s13
	s_lshl_b32 s13, s66, 5
	s_add_u32 s12, s12, s13
	v_readlane_b32 s32, v255, 52
	v_readlane_b32 s33, v255, 53
	s_add_u32 s32, s32, s12
	s_addc_u32 s33, s33, 0
	s_movk_i32 s1, 0x800
	s_mov_b32 s0, 0x42000000
	s_branch .Lcn_dd_n0xf

; #define LAS __attribute__((address_space(3)))
; __device__ __forceinline__ void p_nsa_f(const Args& a, LAS unsigned char* lds) {
;     for (int u = blockIdx.x; u < 256; u += gridDim.x) { const int bk = u & 7, pr = u >> 3;
; #pragma unroll 1
;         for (int rep = 0; rep < 2; ++rep) nsa_unit(a, lds, bk >> 1, bk & 1, rep ? pr : 63 - pr); }
; }
.Lcn_fnone_n0x:
.LBB0_919:
	s_cmpk_lt_u32 s71, 0x100
	s_cbranch_scc0 .LBB0_773
	s_barrier
	s_branch .LBB0_773

; __device__ __forceinline__ void p0_weights(const Args& a, LAS unsigned char* lds) {
;     ...
;         else if ((r -= I_FD) < 16 * I_MG) { const int up = r / (8 * I_MG); r -= up * 8 * I_MG; const int e = r / I_MG; r -= e * I_MG; W = a.in[up ? I_MWU : I_MWG] + (size_t)e * D * DFE; w.K = D; w.N = DFE;
;             w.dst = a.ws + WS_MGU_T + (size_t)e * 2 * DFE * D * (MOE_FP8 ? 1 : 2); w.kind = 2 + up; w.f8 = MOE_FP8; w.scale = F8_WGU; }
;         else { r -= 16 * I_MG; const int e = r / I_MD; r -= e * I_MD; W = a.in[I_MWD] + (size_t)e * DFE * D; w.K = DFE; w.N = D; w.dst = a.ws + WS_MD_T + (size_t)e * D * DFE * (MOE_FP8 ? 1 : 2); w.f8 = MOE_FP8; w.scale = F8_WD; }
;         const int nblk = (w.N + 31) >> 5, kb = r / nblk, nb = r - kb * nblk;
;         w.k0 = 128 * kb + 16 * (lane >> 3); w.n = 32 * nb + 4 * (lane & 7); w.valid = w.n < w.N; w.src = W + (size_t)w.k0 * w.N + w.n;
; __device__ __forceinline__ void nsa_unit(const Args& a, LAS unsigned char* lds, int b, int kvh, int qb) {
;     ...
; #pragma unroll
;     for (int dt = 0; dt < 4; ++dt)
; #pragma unroll
;         for (int i = 0; i < 16; ++i) o[dt][i] = 0.f;
;     float mrun = -1e30f, lrun = 0.f;
;     f32x16 p0, p1;
; #pragma unroll
;     for (int i = 0; i < 16; ++i) { p0[i] = 0.f; p1[i] = 0.f; }
;     bf16x8 pf[2][2];
;     if (w >= 4) asm volatile("s_barrier" ::: "memory");
.LBB0_1840:
	s_cmp_lt_i32 s17, -1
	s_cbranch_scc1 .LBB0_1865
	v_mov_b32_e32 v49, v47
	s_lshl_b32 s0, s62, 1
	s_max_i32 s1, s62, 8
	v_mov_b32_e32 v60, v47
	v_mov_b32_e32 v61, v47
	v_lshl_add_u64 v[206:207], s[30:31], 0, v[48:49]
	s_sub_i32 s69, s0, s1
	v_mov_b32_e32 v46, v47
	v_mov_b32_e32 v48, v47
	v_mov_b32_e32 v50, v47
	v_mov_b32_e32 v51, v47
	v_mov_b32_e32 v52, v47
	v_mov_b32_e32 v53, v47
	v_mov_b32_e32 v54, v47
	v_mov_b32_e32 v55, v47
	v_mov_b32_e32 v56, v47
	v_mov_b32_e32 v57, v47
	v_mov_b32_e32 v58, v47
	v_mov_b32_e32 v59, v47
	v_mov_b64_e32 v[108:109], v[60:61]
	v_mov_b64_e32 v[124:125], v[60:61]
	v_mov_b64_e32 v[140:141], v[60:61]
	v_mov_b64_e32 v[156:157], v[60:61]
	v_mov_b64_e32 v[76:77], v[60:61]
	v_mov_b64_e32 v[92:93], v[60:61]
	v_add_u32_e32 v43, 1, v249
	s_add_i32 s56, s69, 11
	s_add_i32 s57, s69, 10
	s_mov_b32 s68, 2
	s_add_i32 s69, s69, 2
	s_mov_b32 s70, 0
	v_mov_b32_e32 v208, 0xf149f2ca
	v_mov_b32_e32 v209, 0
	s_movk_i32 s71, 0xc000
	v_mov_b64_e32 v[106:107], v[58:59]
	v_mov_b64_e32 v[104:105], v[56:57]
	v_mov_b64_e32 v[102:103], v[54:55]
	v_mov_b64_e32 v[100:101], v[52:53]
	v_mov_b64_e32 v[98:99], v[50:51]
	v_mov_b64_e32 v[96:97], v[48:49]
	v_mov_b64_e32 v[94:95], v[46:47]
	v_mov_b64_e32 v[122:123], v[58:59]
	v_mov_b64_e32 v[120:121], v[56:57]
	v_mov_b64_e32 v[118:119], v[54:55]
	v_mov_b64_e32 v[116:117], v[52:53]
	v_mov_b64_e32 v[114:115], v[50:51]
	v_mov_b64_e32 v[112:113], v[48:49]
	v_mov_b64_e32 v[110:111], v[46:47]
	v_mov_b64_e32 v[138:139], v[58:59]
	v_mov_b64_e32 v[136:137], v[56:57]
	v_mov_b64_e32 v[134:135], v[54:55]
	v_mov_b64_e32 v[132:133], v[52:53]
	v_mov_b64_e32 v[130:131], v[50:51]
	v_mov_b64_e32 v[128:129], v[48:49]
	v_mov_b64_e32 v[126:127], v[46:47]
	v_mov_b64_e32 v[154:155], v[58:59]
	v_mov_b64_e32 v[152:153], v[56:57]
	v_mov_b64_e32 v[150:151], v[54:55]
	v_mov_b64_e32 v[148:149], v[52:53]
	v_mov_b64_e32 v[146:147], v[50:51]
	v_mov_b64_e32 v[144:145], v[48:49]
	v_mov_b64_e32 v[142:143], v[46:47]
	v_mov_b64_e32 v[74:75], v[58:59]
	v_mov_b64_e32 v[72:73], v[56:57]
	v_mov_b64_e32 v[70:71], v[54:55]
	v_mov_b64_e32 v[68:69], v[52:53]
	v_mov_b64_e32 v[66:67], v[50:51]
	v_mov_b64_e32 v[64:65], v[48:49]
	v_mov_b64_e32 v[62:63], v[46:47]
	v_mov_b64_e32 v[90:91], v[58:59]
	v_mov_b64_e32 v[88:89], v[56:57]
	v_mov_b64_e32 v[86:87], v[54:55]
	v_mov_b64_e32 v[84:85], v[52:53]
	v_mov_b64_e32 v[82:83], v[50:51]
	v_mov_b64_e32 v[80:81], v[48:49]
	v_mov_b64_e32 v[78:79], v[46:47]
	s_mov_b32 s67, 0
	s_and_b32 s14, s101, 3
	s_lshl_b32 s14, s14, 28
	s_andn2_b32 s101, s101, 0x30000000
	s_or_b32 s101, s101, s14
	s_and_b32 s14, s101, 0xfffffff
	s_cmp_ge_u32 s14, 168
	s_cbranch_scc1 .Lcn_ldum_n1s
	s_and_b32 s14, s101, 0xfffffff
	s_lshr_b32 s15, s14, 2
	s_lshl_b32 s15, s15, 11
	s_add_u32 s15, s15, s100
	s_lshr_b32 vcc_lo, s15, 9
	s_mul_i32 vcc_lo, vcc_lo, 0x2493
	s_lshr_b32 vcc_lo, vcc_lo, 16
	s_mul_i32 vcc_hi, vcc_lo, 0xe00
	s_sub_u32 s15, s15, vcc_hi
	s_and_b32 s14, s14, 3
	s_cmp_ge_u32 vcc_lo, 16
	s_cbranch_scc1 .Lcn_dn_n1ss
	s_lshr_b32 vcc_hi, s15, 5
	s_mul_i32 vcc_hi, vcc_hi, 0x2493
	s_lshr_b32 vcc_hi, vcc_hi, 16
	s_mul_i32 s0, vcc_hi, 0xe0
	s_sub_u32 s0, s15, s0
	s_lshl_b32 vcc_hi, vcc_hi, 2
	s_add_u32 vcc_hi, vcc_hi, s14
	s_lshr_b32 s15, vcc_lo, 1
	s_and_b32 vcc_lo, vcc_lo, 1
	s_mul_i32 s14, s15, 0x3800000
	s_mul_i32 s15, vcc_hi, 0xe0000
	s_add_u32 s14, s14, s15
	s_lshl_b32 s15, s0, 7
	s_add_u32 s14, s14, s15
	v_readlane_b32 s32, v255, 46
	v_readlane_b32 s33, v255, 47
	s_cmp_eq_u32 vcc_lo, 0
	s_cselect_b32 s32, s98, s32
	s_cselect_b32 s33, s99, s33
	s_add_u32 s32, s32, s14
	s_addc_u32 s33, s33, 0
	s_movk_i32 s1, 0x7000
	s_branch .Lcn_dd_n1ss
.Lcn_dn_n1ss:
	s_lshr_b32 vcc_hi, s15, 6
	s_and_b32 s0, s15, 63
	s_lshl_b32 vcc_hi, vcc_hi, 2
	s_add_u32 vcc_hi, vcc_hi, s14
	s_sub_u32 s15, vcc_lo, 16
	s_mul_i32 s14, s15, 0x3800000
	s_lshl_b32 s15, vcc_hi, 18
	s_add_u32 s14, s14, s15
	s_lshl_b32 s15, s0, 7
	s_add_u32 s14, s14, s15
	v_readlane_b32 s32, v255, 48
	v_readlane_b32 s33, v255, 49
	s_add_u32 s32, s32, s14
	s_addc_u32 s33, s33, 0
	s_movk_i32 s1, 0x2000

; __device__ __forceinline__ void witem_load(const WItem& w, f32x4 (&v)[16]) {
;     if (!w.valid) return;
; #pragma unroll
;     for (int i = 0; i < 16; ++i) v[i] = *(const f32x4*)(w.src + (size_t)i * w.N);
; }
.Lcn_lgo_n1s:
	v_and_b32_e32 v220, 63, v0
	v_and_b32_e32 v253, 7, v220
	v_lshrrev_b32_e32 v220, 3, v220
	v_lshlrev_b32_e32 v220, 2, v220
	v_lshlrev_b32_e32 v221, 4, v253
	v_lshlrev_b32_e32 v253, 2, v253
	v_mad_u32_u24 v254, v220, s1, v221
	global_load_dwordx4 v[212:215], v254, s[32:33] nt
	s_add_u32 s32, s32, s1
	s_addc_u32 s33, s33, 0
	global_load_dwordx4 v[216:219], v254, s[32:33] nt
	s_add_u32 s32, s32, s1
	s_addc_u32 s33, s33, 0
	global_load_dwordx4 v[224:227], v254, s[32:33] nt
	s_add_u32 s32, s32, s1
	s_addc_u32 s33, s33, 0
	global_load_dwordx2 v[220:221], v254, s[32:33] offset:0 nt
	global_load_dword v253, v254, s[32:33] offset:8 nt
	global_load_dword v254, v254, s[32:33] offset:12 nt
	s_branch .LBB0_1843

; __device__ __forceinline__ unsigned pk4_fp8(float a, float b, float c, float d) { int p = __builtin_amdgcn_cvt_pk_fp8_f32(a, b, 0, false); p = __builtin_amdgcn_cvt_pk_fp8_f32(c, d, p, true); return (unsigned)p; }
; __device__ __forceinline__ void witem_store(const WItem& w, const f32x4 (&v)[16]) {
;     if (!w.valid) return;
;     if (w.f8) {
; #pragma unroll
;         for (int j = 0; j < 4; ++j) { u32x4 o; const float sc = w.scale;
;             o.x = pk4_fp8(v[0][j] * sc, v[1][j] * sc, v[2][j] * sc, v[3][j] * sc); o.y = pk4_fp8(v[4][j] * sc, v[5][j] * sc, v[6][j] * sc, v[7][j] * sc);
;             o.z = pk4_fp8(v[8][j] * sc, v[9][j] * sc, v[10][j] * sc, v[11][j] * sc); o.w = pk4_fp8(v[12][j] * sc, v[13][j] * sc, v[14][j] * sc, v[15][j] * sc);
;             *(u32x4*)(w.dst + (size_t)witem_row(w.kind, w.n + j) * w.K + w.k0) = o; }
; __device__ __forceinline__ void p0_weights(const Args& a, LAS unsigned char* lds) {
;     ...
;         else if ((r -= I_FD) < 16 * I_MG) { const int up = r / (8 * I_MG); r -= up * 8 * I_MG; const int e = r / I_MG; r -= e * I_MG; W = a.in[up ? I_MWU : I_MWG] + (size_t)e * D * DFE; w.K = D; w.N = DFE;
;             w.dst = a.ws + WS_MGU_T + (size_t)e * 2 * DFE * D * (MOE_FP8 ? 1 : 2); w.kind = 2 + up; w.f8 = MOE_FP8; w.scale = F8_WGU; }
;         else { r -= 16 * I_MG; const int e = r / I_MD; r -= e * I_MD; W = a.in[I_MWD] + (size_t)e * DFE * D; w.K = DFE; w.N = D; w.dst = a.ws + WS_MD_T + (size_t)e * D * DFE * (MOE_FP8 ? 1 : 2); w.f8 = MOE_FP8; w.scale = F8_WD; }
;         const int nblk = (w.N + 31) >> 5, kb = r / nblk, nb = r - kb * nblk;
;         w.k0 = 128 * kb + 16 * (lane >> 3); w.n = 32 * nb + 4 * (lane & 7); w.valid = w.n < w.N; w.src = W + (size_t)w.k0 * w.N + w.n;
.Lcn_wd_n1:
	s_bitcmp1_b32 s25, 31
	s_cbranch_scc0 .Lcn_snone_n1l
	s_and_b32 s14, s25, 0xfffffff
	s_lshr_b32 s15, s14, 2
	s_lshl_b32 s15, s15, 11
	s_add_u32 s15, s15, s100
	s_lshr_b32 vcc_lo, s15, 9
	s_mul_i32 vcc_lo, vcc_lo, 0x2493
	s_lshr_b32 vcc_lo, vcc_lo, 16
	s_mul_i32 vcc_hi, vcc_lo, 0xe00
	s_sub_u32 s15, s15, vcc_hi
	s_and_b32 s14, s14, 3
	s_cmp_ge_u32 vcc_lo, 16
	s_cbranch_scc1 .Lcn_dn_n1ld
	s_lshr_b32 vcc_hi, s15, 5
	s_mul_i32 vcc_hi, vcc_hi, 0x2493
	s_lshr_b32 vcc_hi, vcc_hi, 16
	s_mul_i32 s0, vcc_hi, 0xe0
	s_sub_u32 s0, s15, s0
	s_lshl_b32 vcc_hi, vcc_hi, 2
	s_add_u32 vcc_hi, vcc_hi, s14
	s_lshr_b32 s15, vcc_lo, 1
	s_and_b32 vcc_lo, vcc_lo, 1
	s_mul_i32 s14, s15, 0x1c00000
	s_add_u32 s14, s14, 0x4a000000
	s_lshr_b32 s15, s0, 2
	s_lshl_b32 s15, s15, 8
	s_lshl_b32 vcc_lo, vcc_lo, 7
	s_add_u32 s15, s15, vcc_lo
	s_and_b32 vcc_lo, s0, 3
	s_lshl_b32 vcc_lo, vcc_lo, 5
	s_add_u32 s15, s15, vcc_lo
	s_lshl_b32 s15, s15, 11
	s_add_u32 s14, s14, s15
	s_lshl_b32 s15, vcc_hi, 5
	s_add_u32 s14, s14, s15
	v_readlane_b32 s32, v255, 52
	v_readlane_b32 s33, v255, 53
	s_add_u32 s32, s32, s14
	s_addc_u32 s33, s33, 0
	s_movk_i32 s1, 0x800
	s_mov_b32 s0, 0x42000000
	s_branch .Lcn_dd_n1ld
.Lcn_dn_n1ld:
	s_lshr_b32 vcc_hi, s15, 6
	s_and_b32 s0, s15, 63
	s_lshl_b32 vcc_hi, vcc_hi, 2
	s_add_u32 vcc_hi, vcc_hi, s14
	s_sub_u32 s15, vcc_lo, 16
	s_mul_i32 s14, s15, 0xe00000
	s_add_u32 s14, s14, 0x66000000
	s_mul_i32 s15, s0, 0x38000
	s_add_u32 s14, s14, s15
	s_lshl_b32 s15, vcc_hi, 5
	s_add_u32 s14, s14, s15
	v_readlane_b32 s32, v255, 52
	v_readlane_b32 s33, v255, 53
	s_add_u32 s32, s32, s14
	s_addc_u32 s33, s33, 0
	s_movk_i32 s1, 0x1c00
	s_mov_b32 s0, 0x43000000
.Lcn_dd_n1ld:
	v_mul_f32_e32 v212, s0, v212
	v_mul_f32_e32 v213, s0, v213
	v_mul_f32_e32 v214, s0, v214
	v_mul_f32_e32 v215, s0, v215
	v_mul_f32_e32 v216, s0, v216
	v_mul_f32_e32 v217, s0, v217
	v_mul_f32_e32 v218, s0, v218
	v_mul_f32_e32 v219, s0, v219
	v_mul_f32_e32 v224, s0, v224
	v_mul_f32_e32 v225, s0, v225
	v_mul_f32_e32 v226, s0, v226
	v_mul_f32_e32 v227, s0, v227
	v_mul_f32_e32 v220, s0, v220
	v_mul_f32_e32 v221, s0, v221
	v_mul_f32_e32 v253, s0, v253
	v_mul_f32_e32 v254, s0, v254
	v_cvt_pk_fp8_f32 v212, v212, v216
	v_cvt_pk_fp8_f32 v213, v213, v217
	v_cvt_pk_fp8_f32 v214, v214, v218
	v_cvt_pk_fp8_f32 v215, v215, v219
	v_cvt_pk_fp8_f32 v212, v224, v220 op_sel:[0,0,1]
	v_cvt_pk_fp8_f32 v213, v225, v221 op_sel:[0,0,1]
	v_cvt_pk_fp8_f32 v214, v226, v253 op_sel:[0,0,1]
	v_cvt_pk_fp8_f32 v215, v227, v254 op_sel:[0,0,1]
	s_and_b32 s14, s25, 3
	v_and_b32_e32 v216, 63, v0
	v_and_b32_e32 v217, 7, v216
	v_lshrrev_b32_e32 v216, 3, v216
	v_and_b32_e32 v218, 3, v217
	v_xor_b32_e32 v218, s14, v218
	v_lshlrev_b32_e32 v218, 5, v218
	v_lshl_add_u32 v218, v216, 2, v218
	v_lshl_add_u32 v218, v217, 9, v218
	v_and_b32_e32 v219, 0x1c0, v0
	v_lshl_add_u32 v218, v219, 6, v218
	v_add_u32_e32 v218, 0x1c000, v218
	ds_write_b32 v218, v212 offset:0
	ds_write_b32 v218, v213 offset:128
	ds_write_b32 v218, v214 offset:256
	ds_write_b32 v218, v215 offset:384
	s_mov_b32 s67, s25
	s_mov_b32 s25, 0
.Lcn_snone_n1l:
	s_and_b32 s14, s67, 0x80000003
	s_cmp_eq_u32 s14, 0x80000003
	s_cbranch_scc0 .Lcn_fnone_n1l
	s_bitcmp1_b32 s67, 31
	s_cbranch_scc0 .Lcn_fnone_n1l
	s_and_b32 s14, s67, 0xfffffff
	s_lshr_b32 s15, s14, 2
	s_lshl_b32 s15, s15, 11
	s_add_u32 s15, s15, s100
	s_lshr_b32 vcc_lo, s15, 9
	s_mul_i32 vcc_lo, vcc_lo, 0x2493
	s_lshr_b32 vcc_lo, vcc_lo, 16
	s_mul_i32 vcc_hi, vcc_lo, 0xe00
	s_sub_u32 s15, s15, vcc_hi
	s_mov_b32 s14, 0
	s_cmp_ge_u32 vcc_lo, 16
	s_cbranch_scc1 .Lcn_dn_n1lf
	s_lshr_b32 vcc_hi, s15, 5
	s_mul_i32 vcc_hi, vcc_hi, 0x2493
	s_lshr_b32 vcc_hi, vcc_hi, 16
	s_mul_i32 s0, vcc_hi, 0xe0
	s_sub_u32 s0, s15, s0
	s_lshl_b32 vcc_hi, vcc_hi, 2
	s_add_u32 vcc_hi, vcc_hi, s14
	s_lshr_b32 s15, vcc_lo, 1
	s_and_b32 vcc_lo, vcc_lo, 1
	s_mul_i32 s14, s15, 0x1c00000
	s_add_u32 s14, s14, 0x4a000000
	s_lshr_b32 s15, s0, 2
	s_lshl_b32 s15, s15, 8
	s_lshl_b32 vcc_lo, vcc_lo, 7
	s_add_u32 s15, s15, vcc_lo
	s_and_b32 vcc_lo, s0, 3
	s_lshl_b32 vcc_lo, vcc_lo, 5
	s_add_u32 s15, s15, vcc_lo
	s_lshl_b32 s15, s15, 11
	s_add_u32 s14, s14, s15
	s_lshl_b32 s15, vcc_hi, 5
	s_add_u32 s14, s14, s15
	v_readlane_b32 s32, v255, 52
	v_readlane_b32 s33, v255, 53
	s_add_u32 s32, s32, s14
	s_addc_u32 s33, s33, 0
	s_movk_i32 s1, 0x800
	s_mov_b32 s0, 0x42000000
	s_branch .Lcn_dd_n1lf

; __device__ __forceinline__ unsigned pk4_fp8(float a, float b, float c, float d) { int p = __builtin_amdgcn_cvt_pk_fp8_f32(a, b, 0, false); p = __builtin_amdgcn_cvt_pk_fp8_f32(c, d, p, true); return (unsigned)p; }
; __device__ __forceinline__ void witem_store(const WItem& w, const f32x4 (&v)[16]) {
;     if (!w.valid) return;
;     if (w.f8) {
; #pragma unroll
;         for (int j = 0; j < 4; ++j) { u32x4 o; const float sc = w.scale;
;             o.x = pk4_fp8(v[0][j] * sc, v[1][j] * sc, v[2][j] * sc, v[3][j] * sc); o.y = pk4_fp8(v[4][j] * sc, v[5][j] * sc, v[6][j] * sc, v[7][j] * sc);
;             o.z = pk4_fp8(v[8][j] * sc, v[9][j] * sc, v[10][j] * sc, v[11][j] * sc); o.w = pk4_fp8(v[12][j] * sc, v[13][j] * sc, v[14][j] * sc, v[15][j] * sc);
;             *(u32x4*)(w.dst + (size_t)witem_row(w.kind, w.n + j) * w.K + w.k0) = o; }
; __device__ __forceinline__ void p0_weights(const Args& a, LAS unsigned char* lds) {
;     ...
;     { f32x4 v[16], vn[16];
;       WItem cur = decode(gw); witem_load(cur, v);
; #pragma unroll 1
;       for (int it = gw; it < NIT; it += NGW) {
;           const WItem nxt = decode(it + NGW); witem_load(nxt, vn);
;           __builtin_amdgcn_sched_barrier(0);
;           witem_store(cur, v);
;           __builtin_amdgcn_sched_barrier(0);
; #pragma unroll
;           for (int i = 0; i < 16; ++i) v[i] = vn[i];
;           cur = nxt; } }
.Lcn_dd_n1lf:
	s_lshr_b32 s14, s101, 28
	s_and_b32 s14, s14, 3
	s_and_b32 s15, s67, 3
	s_add_u32 s15, s15, 1
	s_sub_u32 s15, s15, s14
	v_and_b32_e32 v220, 63, v0
	v_lshrrev_b32_e32 v221, 3, v220
	v_and_b32_e32 v220, 7, v220
	v_lshrrev_b32_e32 v253, 1, v220
	v_subrev_u32_e32 v254, s14, v253
	v_cmp_gt_u32_e32 vcc, s15, v254
	v_lshrrev_b32_e32 v254, 2, v221
	v_xor_b32_e32 v254, v254, v253
	v_lshlrev_b32_e32 v254, 1, v254
	v_and_b32_e32 v253, 1, v220
	v_or_b32_e32 v254, v254, v253
	v_lshlrev_b32_e32 v254, 4, v254
	v_lshl_add_u32 v254, v221, 7, v254
	v_and_b32_e32 v253, 0x1c0, v0
	v_lshl_add_u32 v254, v253, 6, v254
	v_add_u32_e32 v254, 0x1c000, v254
	v_xor_b32_e32 v253, 64, v254
	v_mul_u32_u24_e32 v221, s1, v221
	v_lshl_add_u32 v221, v220, 4, v221
	s_and_saveexec_b64 s[14:15], vcc
	ds_read_b128 v[212:215], v254
	ds_read_b128 v[216:219], v253 offset:1024
	ds_read_b128 v[224:227], v254 offset:2048
	s_lshl_b32 s1, s1, 3
	s_waitcnt lgkmcnt(0)
	global_store_dwordx4 v221, v[212:215], s[32:33] nt
	s_add_u32 s32, s32, s1
	s_addc_u32 s33, s33, 0
	s_nop 1
	ds_read_b128 v[212:215], v253 offset:3072
	global_store_dwordx4 v221, v[216:219], s[32:33] nt
	s_add_u32 s32, s32, s1
	s_addc_u32 s33, s33, 0
	global_store_dwordx4 v221, v[224:227], s[32:33] nt
	s_add_u32 s32, s32, s1
	s_addc_u32 s33, s33, 0
	s_waitcnt lgkmcnt(0)
	global_store_dwordx4 v221, v[212:215], s[32:33] nt
	s_mov_b64 exec, s[14:15]
	s_and_b32 vcc_lo, s67, 3
	s_add_u32 vcc_lo, vcc_lo, 1
	s_and_b32 vcc_lo, vcc_lo, 3
	s_lshl_b32 vcc_lo, vcc_lo, 28
	s_andn2_b32 s101, s101, 0x30000000
	s_or_b32 s101, s101, vcc_lo
	s_mov_b32 s67, 0
.Lcn_fnone_n1l:
	s_mov_b32 s25, 0
	s_cmp_gt_i32 s70, s17
	s_cbranch_scc1 .Lcn_lskip_n1l
	s_and_b32 s14, s101, 0xfffffff
	s_cmp_ge_u32 s14, 168
	s_cbranch_scc1 .Lcn_ldum_n1l
	s_and_b32 s14, s101, 0xfffffff
	s_lshr_b32 s15, s14, 2
	s_lshl_b32 s15, s15, 11
	s_add_u32 s15, s15, s100
	s_lshr_b32 vcc_lo, s15, 9
	s_mul_i32 vcc_lo, vcc_lo, 0x2493
	s_lshr_b32 vcc_lo, vcc_lo, 16
	s_mul_i32 vcc_hi, vcc_lo, 0xe00
	s_sub_u32 s15, s15, vcc_hi
	s_and_b32 s14, s14, 3
	s_cmp_ge_u32 vcc_lo, 16
	s_cbranch_scc1 .Lcn_dn_n1ls
	s_lshr_b32 vcc_hi, s15, 5
	s_mul_i32 vcc_hi, vcc_hi, 0x2493
	s_lshr_b32 vcc_hi, vcc_hi, 16
	s_mul_i32 s0, vcc_hi, 0xe0
	s_sub_u32 s0, s15, s0
	s_lshl_b32 vcc_hi, vcc_hi, 2
	s_add_u32 vcc_hi, vcc_hi, s14
	s_lshr_b32 s15, vcc_lo, 1
	s_and_b32 vcc_lo, vcc_lo, 1
	s_mul_i32 s14, s15, 0x3800000
	s_mul_i32 s15, vcc_hi, 0xe0000
	s_add_u32 s14, s14, s15
	s_lshl_b32 s15, s0, 7
	s_add_u32 s14, s14, s15
	v_readlane_b32 s32, v255, 46
	v_readlane_b32 s33, v255, 47
	s_cmp_eq_u32 vcc_lo, 0
	s_cselect_b32 s32, s98, s32
	s_cselect_b32 s33, s99, s33
	s_add_u32 s32, s32, s14
	s_addc_u32 s33, s33, 0
	s_movk_i32 s1, 0x7000
	s_branch .Lcn_dd_n1ls

; __device__ __forceinline__ void witem_load(const WItem& w, f32x4 (&v)[16]) {
;     if (!w.valid) return;
; #pragma unroll
;     for (int i = 0; i < 16; ++i) v[i] = *(const f32x4*)(w.src + (size_t)i * w.N);
; }
; __device__ __forceinline__ void nsa_unit(const Args& a, LAS unsigned char* lds, int b, int kvh, int qb) {
;     ...
;     for (int it = 0; it <= nTot; ++it) {
;         if (it + 1 < nTot) asm volatile("s_waitcnt vmcnt(4) lgkmcnt(0)\n\ts_barrier" ::: "memory"); else asm volatile("s_waitcnt vmcnt(0) lgkmcnt(0)\n\ts_barrier" ::: "memory");
.Lcn_lgo_n1l:
	v_and_b32_e32 v220, 63, v0
	v_and_b32_e32 v253, 7, v220
	v_lshrrev_b32_e32 v220, 3, v220
	v_lshlrev_b32_e32 v220, 2, v220
	v_lshlrev_b32_e32 v221, 4, v253
	v_lshlrev_b32_e32 v253, 2, v253
	v_mad_u32_u24 v254, v220, s1, v221
	global_load_dwordx4 v[212:215], v254, s[32:33] nt
	s_add_u32 s32, s32, s1
	s_addc_u32 s33, s33, 0
	global_load_dwordx4 v[216:219], v254, s[32:33] nt
	s_add_u32 s32, s32, s1
	s_addc_u32 s33, s33, 0
	global_load_dwordx4 v[224:227], v254, s[32:33] nt
	s_add_u32 s32, s32, s1
	s_addc_u32 s33, s33, 0
	global_load_dwordx2 v[220:221], v254, s[32:33] offset:0 nt
	global_load_dword v253, v254, s[32:33] offset:8 nt
	global_load_dword v254, v254, s[32:33] offset:12 nt
.Lcn_lskip_n1l:
	s_add_i32 s70, s70, 1
	s_addk_i32 s71, 0x4000
	s_add_i32 s68, s68, 1
	s_cmp_eq_u32 s56, s70
	s_cbranch_scc1 .Lcn_exit_n1
.LBB0_1843:
	s_cmp_ge_i32 s70, s17
	s_mov_b64 s[0:1], -1
	s_cbranch_scc0 .LBB0_1846
	s_waitcnt vmcnt(6) lgkmcnt(0)
	s_barrier
	s_cbranch_execz .LBB0_1847

; __device__ __forceinline__ void nsa_unit(const Args& a, LAS unsigned char* lds, int b, int kvh, int qb) {
;     ...
;         if (it + 1 < nTot) asm volatile("s_waitcnt vmcnt(4) lgkmcnt(0)\n\ts_barrier" ::: "memory"); else asm volatile("s_waitcnt vmcnt(0) lgkmcnt(0)\n\ts_barrier" ::: "memory");
;         if (it > 0) { const int ti = it - 1;
.LBB0_1847:
	s_waitcnt vmcnt(10) lgkmcnt(0)
	s_barrier
	s_cmp_lg_u32 s70, 0
	s_cselect_b64 s[0:1], -1, 0
	s_cmp_eq_u32 s70, 0
	s_cbranch_scc1 .LBB0_1858

; __device__ __forceinline__ unsigned pk4_fp8(float a, float b, float c, float d) { int p = __builtin_amdgcn_cvt_pk_fp8_f32(a, b, 0, false); p = __builtin_amdgcn_cvt_pk_fp8_f32(c, d, p, true); return (unsigned)p; }
; __device__ __forceinline__ void witem_store(const WItem& w, const f32x4 (&v)[16]) {
;     if (!w.valid) return;
;     if (w.f8) {
; #pragma unroll
;         for (int j = 0; j < 4; ++j) { u32x4 o; const float sc = w.scale;
;             o.x = pk4_fp8(v[0][j] * sc, v[1][j] * sc, v[2][j] * sc, v[3][j] * sc); o.y = pk4_fp8(v[4][j] * sc, v[5][j] * sc, v[6][j] * sc, v[7][j] * sc);
;             o.z = pk4_fp8(v[8][j] * sc, v[9][j] * sc, v[10][j] * sc, v[11][j] * sc); o.w = pk4_fp8(v[12][j] * sc, v[13][j] * sc, v[14][j] * sc, v[15][j] * sc);
;             *(u32x4*)(w.dst + (size_t)witem_row(w.kind, w.n + j) * w.K + w.k0) = o; }
; __device__ __forceinline__ void p0_weights(const Args& a, LAS unsigned char* lds) {
;     ...
;         else if ((r -= I_FD) < 16 * I_MG) { const int up = r / (8 * I_MG); r -= up * 8 * I_MG; const int e = r / I_MG; r -= e * I_MG; W = a.in[up ? I_MWU : I_MWG] + (size_t)e * D * DFE; w.K = D; w.N = DFE;
;             w.dst = a.ws + WS_MGU_T + (size_t)e * 2 * DFE * D * (MOE_FP8 ? 1 : 2); w.kind = 2 + up; w.f8 = MOE_FP8; w.scale = F8_WGU; }
;         else { r -= 16 * I_MG; const int e = r / I_MD; r -= e * I_MD; W = a.in[I_MWD] + (size_t)e * DFE * D; w.K = DFE; w.N = D; w.dst = a.ws + WS_MD_T + (size_t)e * D * DFE * (MOE_FP8 ? 1 : 2); w.f8 = MOE_FP8; w.scale = F8_WD; }
;         const int nblk = (w.N + 31) >> 5, kb = r / nblk, nb = r - kb * nblk;
;         w.k0 = 128 * kb + 16 * (lane >> 3); w.n = 32 * nb + 4 * (lane & 7); w.valid = w.n < w.N; w.src = W + (size_t)w.k0 * w.N + w.n;
.Lcn_exit_n1:
	s_bitcmp1_b32 s25, 31
	s_cbranch_scc0 .Lcn_xnone_n1
	s_waitcnt vmcnt(0)
	s_bitcmp1_b32 s25, 31
	s_cbranch_scc0 .Lcn_snone_n1x
	s_and_b32 s14, s25, 0xfffffff
	s_lshr_b32 s15, s14, 2
	s_lshl_b32 s15, s15, 11
	s_add_u32 s15, s15, s100
	s_lshr_b32 vcc_lo, s15, 9
	s_mul_i32 vcc_lo, vcc_lo, 0x2493
	s_lshr_b32 vcc_lo, vcc_lo, 16
	s_mul_i32 vcc_hi, vcc_lo, 0xe00
	s_sub_u32 s15, s15, vcc_hi
	s_and_b32 s14, s14, 3
	s_cmp_ge_u32 vcc_lo, 16
	s_cbranch_scc1 .Lcn_dn_n1xd
	s_lshr_b32 vcc_hi, s15, 5
	s_mul_i32 vcc_hi, vcc_hi, 0x2493
	s_lshr_b32 vcc_hi, vcc_hi, 16
	s_mul_i32 s0, vcc_hi, 0xe0
	s_sub_u32 s0, s15, s0
	s_lshl_b32 vcc_hi, vcc_hi, 2
	s_add_u32 vcc_hi, vcc_hi, s14
	s_lshr_b32 s15, vcc_lo, 1
	s_and_b32 vcc_lo, vcc_lo, 1
	s_mul_i32 s14, s15, 0x1c00000
	s_add_u32 s14, s14, 0x4a000000
	s_lshr_b32 s15, s0, 2
	s_lshl_b32 s15, s15, 8
	s_lshl_b32 vcc_lo, vcc_lo, 7
	s_add_u32 s15, s15, vcc_lo
	s_and_b32 vcc_lo, s0, 3
	s_lshl_b32 vcc_lo, vcc_lo, 5
	s_add_u32 s15, s15, vcc_lo
	s_lshl_b32 s15, s15, 11
	s_add_u32 s14, s14, s15
	s_lshl_b32 s15, vcc_hi, 5
	s_add_u32 s14, s14, s15
	v_readlane_b32 s32, v255, 52
	v_readlane_b32 s33, v255, 53
	s_add_u32 s32, s32, s14
	s_addc_u32 s33, s33, 0
	s_movk_i32 s1, 0x800
	s_mov_b32 s0, 0x42000000
	s_branch .Lcn_dd_n1xd

; __device__ __forceinline__ unsigned pk4_fp8(float a, float b, float c, float d) { int p = __builtin_amdgcn_cvt_pk_fp8_f32(a, b, 0, false); p = __builtin_amdgcn_cvt_pk_fp8_f32(c, d, p, true); return (unsigned)p; }
; __device__ __forceinline__ void witem_store(const WItem& w, const f32x4 (&v)[16]) {
;     if (!w.valid) return;
;     if (w.f8) {
; #pragma unroll
;         for (int j = 0; j < 4; ++j) { u32x4 o; const float sc = w.scale;
;             o.x = pk4_fp8(v[0][j] * sc, v[1][j] * sc, v[2][j] * sc, v[3][j] * sc); o.y = pk4_fp8(v[4][j] * sc, v[5][j] * sc, v[6][j] * sc, v[7][j] * sc);
;             o.z = pk4_fp8(v[8][j] * sc, v[9][j] * sc, v[10][j] * sc, v[11][j] * sc); o.w = pk4_fp8(v[12][j] * sc, v[13][j] * sc, v[14][j] * sc, v[15][j] * sc);
;             *(u32x4*)(w.dst + (size_t)witem_row(w.kind, w.n + j) * w.K + w.k0) = o; }
; __device__ __forceinline__ void p0_weights(const Args& a, LAS unsigned char* lds) {
;     ...
;         else if ((r -= I_FD) < 16 * I_MG) { const int up = r / (8 * I_MG); r -= up * 8 * I_MG; const int e = r / I_MG; r -= e * I_MG; W = a.in[up ? I_MWU : I_MWG] + (size_t)e * D * DFE; w.K = D; w.N = DFE;
;             w.dst = a.ws + WS_MGU_T + (size_t)e * 2 * DFE * D * (MOE_FP8 ? 1 : 2); w.kind = 2 + up; w.f8 = MOE_FP8; w.scale = F8_WGU; }
;         else { r -= 16 * I_MG; const int e = r / I_MD; r -= e * I_MD; W = a.in[I_MWD] + (size_t)e * DFE * D; w.K = DFE; w.N = D; w.dst = a.ws + WS_MD_T + (size_t)e * D * DFE * (MOE_FP8 ? 1 : 2); w.f8 = MOE_FP8; w.scale = F8_WD; }
;         const int nblk = (w.N + 31) >> 5, kb = r / nblk, nb = r - kb * nblk;
;         w.k0 = 128 * kb + 16 * (lane >> 3); w.n = 32 * nb + 4 * (lane & 7); w.valid = w.n < w.N; w.src = W + (size_t)w.k0 * w.N + w.n;
.Lcn_snone_n1x:
.Lcn_xnone_n1:
	s_bitcmp1_b32 s67, 31
	s_cbranch_scc0 .Lcn_fnone_n1x
	s_and_b32 s14, s67, 0xfffffff
	s_lshr_b32 s15, s14, 2
	s_lshl_b32 s15, s15, 11
	s_add_u32 s15, s15, s100
	s_lshr_b32 vcc_lo, s15, 9
	s_mul_i32 vcc_lo, vcc_lo, 0x2493
	s_lshr_b32 vcc_lo, vcc_lo, 16
	s_mul_i32 vcc_hi, vcc_lo, 0xe00
	s_sub_u32 s15, s15, vcc_hi
	s_mov_b32 s14, 0
	s_cmp_ge_u32 vcc_lo, 16
	s_cbranch_scc1 .Lcn_dn_n1xf
	s_lshr_b32 vcc_hi, s15, 5
	s_mul_i32 vcc_hi, vcc_hi, 0x2493
	s_lshr_b32 vcc_hi, vcc_hi, 16
	s_mul_i32 s0, vcc_hi, 0xe0
	s_sub_u32 s0, s15, s0
	s_lshl_b32 vcc_hi, vcc_hi, 2
	s_add_u32 vcc_hi, vcc_hi, s14
	s_lshr_b32 s15, vcc_lo, 1
	s_and_b32 vcc_lo, vcc_lo, 1
	s_mul_i32 s14, s15, 0x1c00000
	s_add_u32 s14, s14, 0x4a000000
	s_lshr_b32 s15, s0, 2
	s_lshl_b32 s15, s15, 8
	s_lshl_b32 vcc_lo, vcc_lo, 7
	s_add_u32 s15, s15, vcc_lo
	s_and_b32 vcc_lo, s0, 3
	s_lshl_b32 vcc_lo, vcc_lo, 5
	s_add_u32 s15, s15, vcc_lo
	s_lshl_b32 s15, s15, 11
	s_add_u32 s14, s14, s15
	s_lshl_b32 s15, vcc_hi, 5
	s_add_u32 s14, s14, s15
	v_readlane_b32 s32, v255, 52
	v_readlane_b32 s33, v255, 53
	s_add_u32 s32, s32, s14
	s_addc_u32 s33, s33, 0
	s_movk_i32 s1, 0x800
	s_mov_b32 s0, 0x42000000
	s_branch .Lcn_dd_n1xf

; __device__ __forceinline__ void nsa_unit(const Args& a, LAS unsigned char* lds, int b, int kvh, int qb) {
;     ...
;     if (w < 4) asm volatile("s_barrier" ::: "memory");
;     __syncthreads();
; __device__ __forceinline__ void p_nsa_f(const Args& a, LAS unsigned char* lds) {
;     for (int u = blockIdx.x; u < 256; u += gridDim.x) { const int bk = u & 7, pr = u >> 3;
; #pragma unroll 1
;         for (int rep = 0; rep < 2; ++rep) nsa_unit(a, lds, bk >> 1, bk & 1, rep ? pr : 63 - pr); }
.Lcn_fnone_n1x:
.LBB0_1865:
	s_cmpk_lt_u32 s61, 0x100
	s_cbranch_scc0 .LBB0_1719
	s_barrier
	s_branch .LBB0_1719

; __device__ __forceinline__ void p0_weights(const Args& a, LAS unsigned char* lds) {
;     ...
;         else if ((r -= I_FD) < 16 * I_MG) { const int up = r / (8 * I_MG); r -= up * 8 * I_MG; const int e = r / I_MG; r -= e * I_MG; W = a.in[up ? I_MWU : I_MWG] + (size_t)e * D * DFE; w.K = D; w.N = DFE;
;             w.dst = a.ws + WS_MGU_T + (size_t)e * 2 * DFE * D * (MOE_FP8 ? 1 : 2); w.kind = 2 + up; w.f8 = MOE_FP8; w.scale = F8_WGU; }
;         else { r -= 16 * I_MG; const int e = r / I_MD; r -= e * I_MD; W = a.in[I_MWD] + (size_t)e * DFE * D; w.K = DFE; w.N = D; w.dst = a.ws + WS_MD_T + (size_t)e * D * DFE * (MOE_FP8 ? 1 : 2); w.f8 = MOE_FP8; w.scale = F8_WD; }
;         const int nblk = (w.N + 31) >> 5, kb = r / nblk, nb = r - kb * nblk;
;         w.k0 = 128 * kb + 16 * (lane >> 3); w.n = 32 * nb + 4 * (lane & 7); w.valid = w.n < w.N; w.src = W + (size_t)w.k0 * w.N + w.n;
.LBB0_1880:
.Lcn_left:
	s_and_b32 s8, s101, 0xfffffff
	s_cmp_ge_u32 s8, 168
	s_cbranch_scc1 .Lcn_leftdone
	s_and_b32 s8, s101, 0xfffffff
	s_cmp_ge_u32 s8, 168
	s_cbranch_scc1 .Lcn_ldum_lfA
	s_and_b32 s8, s101, 0xfffffff
	s_lshr_b32 s9, s8, 2
	s_lshl_b32 s9, s9, 11
	s_add_u32 s9, s9, s100
	s_lshr_b32 s10, s9, 9
	s_mul_i32 s10, s10, 0x2493
	s_lshr_b32 s10, s10, 16
	s_mul_i32 s11, s10, 0xe00
	s_sub_u32 s9, s9, s11
	s_and_b32 s8, s8, 3
	s_cmp_ge_u32 s10, 16
	s_cbranch_scc1 .Lcn_dn_lfAs
	s_lshr_b32 s11, s9, 5
	s_mul_i32 s11, s11, 0x2493
	s_lshr_b32 s11, s11, 16
	s_mul_i32 s12, s11, 0xe0
	s_sub_u32 s12, s9, s12
	s_lshl_b32 s11, s11, 2
	s_add_u32 s11, s11, s8
	s_lshr_b32 s9, s10, 1
	s_and_b32 s10, s10, 1
	s_mul_i32 s8, s9, 0x3800000
	s_mul_i32 s9, s11, 0xe0000
	s_add_u32 s8, s8, s9
	s_lshl_b32 s9, s12, 7
	s_add_u32 s8, s8, s9
	v_readlane_b32 s32, v255, 46
	v_readlane_b32 s33, v255, 47
	s_cmp_eq_u32 s10, 0
	s_cselect_b32 s32, s98, s32
	s_cselect_b32 s33, s99, s33
	s_add_u32 s32, s32, s8
	s_addc_u32 s33, s33, 0
	s_movk_i32 s1, 0x7000
	s_branch .Lcn_dd_lfAs
.Lcn_dn_lfAs:
	s_lshr_b32 s11, s9, 6
	s_and_b32 s12, s9, 63
	s_lshl_b32 s11, s11, 2
	s_add_u32 s11, s11, s8
	s_sub_u32 s9, s10, 16
	s_mul_i32 s8, s9, 0x3800000
	s_lshl_b32 s9, s11, 18
	s_add_u32 s8, s8, s9
	s_lshl_b32 s9, s12, 7
	s_add_u32 s8, s8, s9
	v_readlane_b32 s32, v255, 48
	v_readlane_b32 s33, v255, 49
	s_add_u32 s32, s32, s8
	s_addc_u32 s33, s33, 0
	s_movk_i32 s1, 0x2000

; __device__ __forceinline__ void witem_load(const WItem& w, f32x4 (&v)[16]) {
;     if (!w.valid) return;
; #pragma unroll
;     for (int i = 0; i < 16; ++i) v[i] = *(const f32x4*)(w.src + (size_t)i * w.N);
; }
; __device__ __forceinline__ void p0_weights(const Args& a, LAS unsigned char* lds) {
;     ...
;         else if ((r -= I_FD) < 16 * I_MG) { const int up = r / (8 * I_MG); r -= up * 8 * I_MG; const int e = r / I_MG; r -= e * I_MG; W = a.in[up ? I_MWU : I_MWG] + (size_t)e * D * DFE; w.K = D; w.N = DFE;
;             w.dst = a.ws + WS_MGU_T + (size_t)e * 2 * DFE * D * (MOE_FP8 ? 1 : 2); w.kind = 2 + up; w.f8 = MOE_FP8; w.scale = F8_WGU; }
;         else { r -= 16 * I_MG; const int e = r / I_MD; r -= e * I_MD; W = a.in[I_MWD] + (size_t)e * DFE * D; w.K = DFE; w.N = D; w.dst = a.ws + WS_MD_T + (size_t)e * D * DFE * (MOE_FP8 ? 1 : 2); w.f8 = MOE_FP8; w.scale = F8_WD; }
;         const int nblk = (w.N + 31) >> 5, kb = r / nblk, nb = r - kb * nblk;
;         w.k0 = 128 * kb + 16 * (lane >> 3); w.n = 32 * nb + 4 * (lane & 7); w.valid = w.n < w.N; w.src = W + (size_t)w.k0 * w.N + w.n;
.Lcn_lgo_lfA:
	v_and_b32_e32 v112, 63, v0
	v_and_b32_e32 v114, 7, v112
	v_lshrrev_b32_e32 v112, 3, v112
	v_lshlrev_b32_e32 v112, 2, v112
	v_lshlrev_b32_e32 v113, 4, v114
	v_lshlrev_b32_e32 v114, 2, v114
	v_mad_u32_u24 v115, v112, s1, v113
	global_load_dwordx4 v[100:103], v115, s[32:33] nt
	s_add_u32 s32, s32, s1
	s_addc_u32 s33, s33, 0
	global_load_dwordx4 v[104:107], v115, s[32:33] nt
	s_add_u32 s32, s32, s1
	s_addc_u32 s33, s33, 0
	global_load_dwordx4 v[108:111], v115, s[32:33] nt
	s_add_u32 s32, s32, s1
	s_addc_u32 s33, s33, 0
	global_load_dwordx4 v[112:115], v115, s[32:33] nt
	s_and_b32 s8, s101, 0xfffffff
	s_cmp_ge_u32 s8, 168
	s_cbranch_scc1 .Lcn_ldum_lfB
	s_and_b32 s8, s101, 0xfffffff
	s_lshr_b32 s9, s8, 2
	s_lshl_b32 s9, s9, 11
	s_add_u32 s9, s9, s100
	s_lshr_b32 s10, s9, 9
	s_mul_i32 s10, s10, 0x2493
	s_lshr_b32 s10, s10, 16
	s_mul_i32 s11, s10, 0xe00
	s_sub_u32 s9, s9, s11
	s_and_b32 s8, s8, 3
	s_cmp_ge_u32 s10, 16
	s_cbranch_scc1 .Lcn_dn_lfBs
	s_lshr_b32 s11, s9, 5
	s_mul_i32 s11, s11, 0x2493
	s_lshr_b32 s11, s11, 16
	s_mul_i32 s12, s11, 0xe0
	s_sub_u32 s12, s9, s12
	s_lshl_b32 s11, s11, 2
	s_add_u32 s11, s11, s8
	s_lshr_b32 s9, s10, 1
	s_and_b32 s10, s10, 1
	s_mul_i32 s8, s9, 0x3800000
	s_mul_i32 s9, s11, 0xe0000
	s_add_u32 s8, s8, s9
	s_lshl_b32 s9, s12, 7
	s_add_u32 s8, s8, s9
	v_readlane_b32 s32, v255, 46
	v_readlane_b32 s33, v255, 47
	s_cmp_eq_u32 s10, 0
	s_cselect_b32 s32, s98, s32
	s_cselect_b32 s33, s99, s33
	s_add_u32 s32, s32, s8
	s_addc_u32 s33, s33, 0
	s_movk_i32 s1, 0x7000
	s_branch .Lcn_dd_lfBs

; __device__ __forceinline__ void p0_weights(const Args& a, LAS unsigned char* lds) {
;     ...
;     { f32x4 v[16], vn[16];
;       WItem cur = decode(gw); witem_load(cur, v);
; #pragma unroll 1
;       for (int it = gw; it < NIT; it += NGW) {
;           const WItem nxt = decode(it + NGW); witem_load(nxt, vn);
;           __builtin_amdgcn_sched_barrier(0);
;           witem_store(cur, v);
;           __builtin_amdgcn_sched_barrier(0);
; #pragma unroll
;           for (int i = 0; i < 16; ++i) v[i] = vn[i];
;           cur = nxt; } }
.Lcn_dd_lfBs:
	s_and_b32 s26, s101, 0xfffffff
	s_bitset1_b32 s26, 31
	s_add_u32 s101, s101, 1
	s_branch .Lcn_lgo_lfB

; __device__ __forceinline__ void witem_load(const WItem& w, f32x4 (&v)[16]) {
;     if (!w.valid) return;
; #pragma unroll
;     for (int i = 0; i < 16; ++i) v[i] = *(const f32x4*)(w.src + (size_t)i * w.N);
; }
; __device__ __forceinline__ void p0_weights(const Args& a, LAS unsigned char* lds) {
;     ...
;         else if ((r -= I_FD) < 16 * I_MG) { const int up = r / (8 * I_MG); r -= up * 8 * I_MG; const int e = r / I_MG; r -= e * I_MG; W = a.in[up ? I_MWU : I_MWG] + (size_t)e * D * DFE; w.K = D; w.N = DFE;
;             w.dst = a.ws + WS_MGU_T + (size_t)e * 2 * DFE * D * (MOE_FP8 ? 1 : 2); w.kind = 2 + up; w.f8 = MOE_FP8; w.scale = F8_WGU; }
;         else { r -= 16 * I_MG; const int e = r / I_MD; r -= e * I_MD; W = a.in[I_MWD] + (size_t)e * DFE * D; w.K = DFE; w.N = D; w.dst = a.ws + WS_MD_T + (size_t)e * D * DFE * (MOE_FP8 ? 1 : 2); w.f8 = MOE_FP8; w.scale = F8_WD; }
;         const int nblk = (w.N + 31) >> 5, kb = r / nblk, nb = r - kb * nblk;
;         w.k0 = 128 * kb + 16 * (lane >> 3); w.n = 32 * nb + 4 * (lane & 7); w.valid = w.n < w.N; w.src = W + (size_t)w.k0 * w.N + w.n;
.Lcn_lgo_lfB:
	v_and_b32_e32 v128, 63, v0
	v_and_b32_e32 v130, 7, v128
	v_lshrrev_b32_e32 v128, 3, v128
	v_lshlrev_b32_e32 v128, 2, v128
	v_lshlrev_b32_e32 v129, 4, v130
	v_lshlrev_b32_e32 v130, 2, v130
	v_mad_u32_u24 v131, v128, s1, v129
	global_load_dwordx4 v[116:119], v131, s[32:33] nt
	s_add_u32 s32, s32, s1
	s_addc_u32 s33, s33, 0
	global_load_dwordx4 v[120:123], v131, s[32:33] nt
	s_add_u32 s32, s32, s1
	s_addc_u32 s33, s33, 0
	global_load_dwordx4 v[124:127], v131, s[32:33] nt
	s_add_u32 s32, s32, s1
	s_addc_u32 s33, s33, 0
	global_load_dwordx4 v[128:131], v131, s[32:33] nt
	s_and_b32 s8, s101, 0xfffffff
	s_cmp_ge_u32 s8, 168
	s_cbranch_scc1 .Lcn_ldum_lfC
	s_and_b32 s8, s101, 0xfffffff
	s_lshr_b32 s9, s8, 2
	s_lshl_b32 s9, s9, 11
	s_add_u32 s9, s9, s100
	s_lshr_b32 s10, s9, 9
	s_mul_i32 s10, s10, 0x2493
	s_lshr_b32 s10, s10, 16
	s_mul_i32 s11, s10, 0xe00
	s_sub_u32 s9, s9, s11
	s_and_b32 s8, s8, 3
	s_cmp_ge_u32 s10, 16
	s_cbranch_scc1 .Lcn_dn_lfCs
	s_lshr_b32 s11, s9, 5
	s_mul_i32 s11, s11, 0x2493
	s_lshr_b32 s11, s11, 16
	s_mul_i32 s12, s11, 0xe0
	s_sub_u32 s12, s9, s12
	s_lshl_b32 s11, s11, 2
	s_add_u32 s11, s11, s8
	s_lshr_b32 s9, s10, 1
	s_and_b32 s10, s10, 1
	s_mul_i32 s8, s9, 0x3800000
	s_mul_i32 s9, s11, 0xe0000
	s_add_u32 s8, s8, s9
	s_lshl_b32 s9, s12, 7
	s_add_u32 s8, s8, s9
	v_readlane_b32 s32, v255, 46
	v_readlane_b32 s33, v255, 47
	s_cmp_eq_u32 s10, 0
	s_cselect_b32 s32, s98, s32
	s_cselect_b32 s33, s99, s33
	s_add_u32 s32, s32, s8
	s_addc_u32 s33, s33, 0
	s_movk_i32 s1, 0x7000
	s_branch .Lcn_dd_lfCs

; __device__ __forceinline__ void p0_weights(const Args& a, LAS unsigned char* lds) {
;     ...
;     { f32x4 v[16], vn[16];
;       WItem cur = decode(gw); witem_load(cur, v);
; #pragma unroll 1
;       for (int it = gw; it < NIT; it += NGW) {
;           const WItem nxt = decode(it + NGW); witem_load(nxt, vn);
;           __builtin_amdgcn_sched_barrier(0);
;           witem_store(cur, v);
;           __builtin_amdgcn_sched_barrier(0);
; #pragma unroll
;           for (int i = 0; i < 16; ++i) v[i] = vn[i];
;           cur = nxt; } }
.Lcn_dd_lfCs:
	s_and_b32 s27, s101, 0xfffffff
	s_bitset1_b32 s27, 31
	s_add_u32 s101, s101, 1
	s_branch .Lcn_lgo_lfC

; __device__ __forceinline__ void witem_load(const WItem& w, f32x4 (&v)[16]) {
;     if (!w.valid) return;
; #pragma unroll
;     for (int i = 0; i < 16; ++i) v[i] = *(const f32x4*)(w.src + (size_t)i * w.N);
; }
; __device__ __forceinline__ void p0_weights(const Args& a, LAS unsigned char* lds) {
;     ...
;         else if ((r -= I_FD) < 16 * I_MG) { const int up = r / (8 * I_MG); r -= up * 8 * I_MG; const int e = r / I_MG; r -= e * I_MG; W = a.in[up ? I_MWU : I_MWG] + (size_t)e * D * DFE; w.K = D; w.N = DFE;
;             w.dst = a.ws + WS_MGU_T + (size_t)e * 2 * DFE * D * (MOE_FP8 ? 1 : 2); w.kind = 2 + up; w.f8 = MOE_FP8; w.scale = F8_WGU; }
;         else { r -= 16 * I_MG; const int e = r / I_MD; r -= e * I_MD; W = a.in[I_MWD] + (size_t)e * DFE * D; w.K = DFE; w.N = D; w.dst = a.ws + WS_MD_T + (size_t)e * D * DFE * (MOE_FP8 ? 1 : 2); w.f8 = MOE_FP8; w.scale = F8_WD; }
;         const int nblk = (w.N + 31) >> 5, kb = r / nblk, nb = r - kb * nblk;
;         w.k0 = 128 * kb + 16 * (lane >> 3); w.n = 32 * nb + 4 * (lane & 7); w.valid = w.n < w.N; w.src = W + (size_t)w.k0 * w.N + w.n;
.Lcn_lgo_lfC:
	v_and_b32_e32 v144, 63, v0
	v_and_b32_e32 v146, 7, v144
	v_lshrrev_b32_e32 v144, 3, v144
	v_lshlrev_b32_e32 v144, 2, v144
	v_lshlrev_b32_e32 v145, 4, v146
	v_lshlrev_b32_e32 v146, 2, v146
	v_mad_u32_u24 v147, v144, s1, v145
	global_load_dwordx4 v[132:135], v147, s[32:33] nt
	s_add_u32 s32, s32, s1
	s_addc_u32 s33, s33, 0
	global_load_dwordx4 v[136:139], v147, s[32:33] nt
	s_add_u32 s32, s32, s1
	s_addc_u32 s33, s33, 0
	global_load_dwordx4 v[140:143], v147, s[32:33] nt
	s_add_u32 s32, s32, s1
	s_addc_u32 s33, s33, 0
	global_load_dwordx4 v[144:147], v147, s[32:33] nt
	s_and_b32 s8, s101, 0xfffffff
	s_cmp_ge_u32 s8, 168
	s_cbranch_scc1 .Lcn_ldum_lfD
	s_and_b32 s8, s101, 0xfffffff
	s_lshr_b32 s9, s8, 2
	s_lshl_b32 s9, s9, 11
	s_add_u32 s9, s9, s100
	s_lshr_b32 s10, s9, 9
	s_mul_i32 s10, s10, 0x2493
	s_lshr_b32 s10, s10, 16
	s_mul_i32 s11, s10, 0xe00
	s_sub_u32 s9, s9, s11
	s_and_b32 s8, s8, 3
	s_cmp_ge_u32 s10, 16
	s_cbranch_scc1 .Lcn_dn_lfDs
	s_lshr_b32 s11, s9, 5
	s_mul_i32 s11, s11, 0x2493
	s_lshr_b32 s11, s11, 16
	s_mul_i32 s12, s11, 0xe0
	s_sub_u32 s12, s9, s12
	s_lshl_b32 s11, s11, 2
	s_add_u32 s11, s11, s8
	s_lshr_b32 s9, s10, 1
	s_and_b32 s10, s10, 1
	s_mul_i32 s8, s9, 0x3800000
	s_mul_i32 s9, s11, 0xe0000
	s_add_u32 s8, s8, s9
	s_lshl_b32 s9, s12, 7
	s_add_u32 s8, s8, s9
	v_readlane_b32 s32, v255, 46
	v_readlane_b32 s33, v255, 47
	s_cmp_eq_u32 s10, 0
	s_cselect_b32 s32, s98, s32
	s_cselect_b32 s33, s99, s33
	s_add_u32 s32, s32, s8
	s_addc_u32 s33, s33, 0
	s_movk_i32 s1, 0x7000
	s_branch .Lcn_dd_lfDs

; __device__ __forceinline__ void p0_weights(const Args& a, LAS unsigned char* lds) {
;     ...
;     { f32x4 v[16], vn[16];
;       WItem cur = decode(gw); witem_load(cur, v);
; #pragma unroll 1
;       for (int it = gw; it < NIT; it += NGW) {
;           const WItem nxt = decode(it + NGW); witem_load(nxt, vn);
;           __builtin_amdgcn_sched_barrier(0);
;           witem_store(cur, v);
;           __builtin_amdgcn_sched_barrier(0);
; #pragma unroll
;           for (int i = 0; i < 16; ++i) v[i] = vn[i];
;           cur = nxt; } }
.Lcn_dd_lfDs:
	s_and_b32 s28, s101, 0xfffffff
	s_bitset1_b32 s28, 31
	s_add_u32 s101, s101, 1
	s_branch .Lcn_lgo_lfD

; __device__ __forceinline__ unsigned pk4_fp8(float a, float b, float c, float d) { int p = __builtin_amdgcn_cvt_pk_fp8_f32(a, b, 0, false); p = __builtin_amdgcn_cvt_pk_fp8_f32(c, d, p, true); return (unsigned)p; }
; __device__ __forceinline__ void witem_store(const WItem& w, const f32x4 (&v)[16]) {
;     if (!w.valid) return;
;     if (w.f8) {
; #pragma unroll
;         for (int j = 0; j < 4; ++j) { u32x4 o; const float sc = w.scale;
;             o.x = pk4_fp8(v[0][j] * sc, v[1][j] * sc, v[2][j] * sc, v[3][j] * sc); o.y = pk4_fp8(v[4][j] * sc, v[5][j] * sc, v[6][j] * sc, v[7][j] * sc);
;             o.z = pk4_fp8(v[8][j] * sc, v[9][j] * sc, v[10][j] * sc, v[11][j] * sc); o.w = pk4_fp8(v[12][j] * sc, v[13][j] * sc, v[14][j] * sc, v[15][j] * sc);
;             *(u32x4*)(w.dst + (size_t)witem_row(w.kind, w.n + j) * w.K + w.k0) = o; }
; __device__ __forceinline__ void p0_weights(const Args& a, LAS unsigned char* lds) {
;     ...
;         else if ((r -= I_FD) < 16 * I_MG) { const int up = r / (8 * I_MG); r -= up * 8 * I_MG; const int e = r / I_MG; r -= e * I_MG; W = a.in[up ? I_MWU : I_MWG] + (size_t)e * D * DFE; w.K = D; w.N = DFE;
;             w.dst = a.ws + WS_MGU_T + (size_t)e * 2 * DFE * D * (MOE_FP8 ? 1 : 2); w.kind = 2 + up; w.f8 = MOE_FP8; w.scale = F8_WGU; }
;         else { r -= 16 * I_MG; const int e = r / I_MD; r -= e * I_MD; W = a.in[I_MWD] + (size_t)e * DFE * D; w.K = DFE; w.N = D; w.dst = a.ws + WS_MD_T + (size_t)e * D * DFE * (MOE_FP8 ? 1 : 2); w.f8 = MOE_FP8; w.scale = F8_WD; }
;         const int nblk = (w.N + 31) >> 5, kb = r / nblk, nb = r - kb * nblk;
;         w.k0 = 128 * kb + 16 * (lane >> 3); w.n = 32 * nb + 4 * (lane & 7); w.valid = w.n < w.N; w.src = W + (size_t)w.k0 * w.N + w.n;
.Lcn_lgo_lfD:
	v_and_b32_e32 v160, 63, v0
	v_and_b32_e32 v162, 7, v160
	v_lshrrev_b32_e32 v160, 3, v160
	v_lshlrev_b32_e32 v160, 2, v160
	v_lshlrev_b32_e32 v161, 4, v162
	v_lshlrev_b32_e32 v162, 2, v162
	v_mad_u32_u24 v163, v160, s1, v161
	global_load_dwordx4 v[148:151], v163, s[32:33] nt
	s_add_u32 s32, s32, s1
	s_addc_u32 s33, s33, 0
	global_load_dwordx4 v[152:155], v163, s[32:33] nt
	s_add_u32 s32, s32, s1
	s_addc_u32 s33, s33, 0
	global_load_dwordx4 v[156:159], v163, s[32:33] nt
	s_add_u32 s32, s32, s1
	s_addc_u32 s33, s33, 0
	global_load_dwordx4 v[160:163], v163, s[32:33] nt
	s_waitcnt vmcnt(0)
	s_bitcmp1_b32 s25, 31
	s_cbranch_scc0 .Lcn_snone_lfA
	s_and_b32 s8, s25, 0xfffffff
	s_lshr_b32 s9, s8, 2
	s_lshl_b32 s9, s9, 11
	s_add_u32 s9, s9, s100
	s_lshr_b32 s10, s9, 9
	s_mul_i32 s10, s10, 0x2493
	s_lshr_b32 s10, s10, 16
	s_mul_i32 s11, s10, 0xe00
	s_sub_u32 s9, s9, s11
	s_and_b32 s8, s8, 3
	s_cmp_ge_u32 s10, 16
	s_cbranch_scc1 .Lcn_dn_lfAd
	s_lshr_b32 s11, s9, 5
	s_mul_i32 s11, s11, 0x2493
	s_lshr_b32 s11, s11, 16
	s_mul_i32 s12, s11, 0xe0
	s_sub_u32 s12, s9, s12
	s_lshl_b32 s11, s11, 2
	s_add_u32 s11, s11, s8
	s_lshr_b32 s9, s10, 1
	s_and_b32 s10, s10, 1
	s_mul_i32 s8, s9, 0x1c00000
	s_add_u32 s8, s8, 0x4a000000
	s_lshr_b32 s9, s12, 2
	s_lshl_b32 s9, s9, 8
	s_lshl_b32 s10, s10, 7
	s_add_u32 s9, s9, s10
	s_and_b32 s10, s12, 3
	s_lshl_b32 s10, s10, 5
	s_add_u32 s9, s9, s10
	s_lshl_b32 s9, s9, 11
	s_add_u32 s8, s8, s9
	s_lshl_b32 s9, s11, 5
	s_add_u32 s8, s8, s9
	v_readlane_b32 s32, v255, 52
	v_readlane_b32 s33, v255, 53
	s_add_u32 s32, s32, s8
	s_addc_u32 s33, s33, 0
	s_movk_i32 s1, 0x800
	s_mov_b32 s0, 0x42000000
	s_branch .Lcn_dd_lfAd
.Lcn_dn_lfAd:
	s_lshr_b32 s11, s9, 6
	s_and_b32 s12, s9, 63
	s_lshl_b32 s11, s11, 2
	s_add_u32 s11, s11, s8
	s_sub_u32 s9, s10, 16
	s_mul_i32 s8, s9, 0xe00000
	s_add_u32 s8, s8, 0x66000000
	s_mul_i32 s9, s12, 0x38000
	s_add_u32 s8, s8, s9
	s_lshl_b32 s9, s11, 5
	s_add_u32 s8, s8, s9
	v_readlane_b32 s32, v255, 52
	v_readlane_b32 s33, v255, 53
	s_add_u32 s32, s32, s8
	s_addc_u32 s33, s33, 0
	s_movk_i32 s1, 0x1c00
	s_mov_b32 s0, 0x43000000
.Lcn_dd_lfAd:
	s_mov_b32 s25, 0
	v_mul_f32_e32 v100, s0, v100
	v_mul_f32_e32 v101, s0, v101
	v_mul_f32_e32 v102, s0, v102
	v_mul_f32_e32 v103, s0, v103
	v_mul_f32_e32 v104, s0, v104
	v_mul_f32_e32 v105, s0, v105
	v_mul_f32_e32 v106, s0, v106
	v_mul_f32_e32 v107, s0, v107
	v_mul_f32_e32 v108, s0, v108
	v_mul_f32_e32 v109, s0, v109
	v_mul_f32_e32 v110, s0, v110
	v_mul_f32_e32 v111, s0, v111
	v_mul_f32_e32 v112, s0, v112
	v_mul_f32_e32 v113, s0, v113
	v_mul_f32_e32 v114, s0, v114
	v_mul_f32_e32 v115, s0, v115
	v_cvt_pk_fp8_f32 v100, v100, v104
	v_cvt_pk_fp8_f32 v101, v101, v105
	v_cvt_pk_fp8_f32 v102, v102, v106
	v_cvt_pk_fp8_f32 v103, v103, v107
	v_cvt_pk_fp8_f32 v100, v108, v112 op_sel:[0,0,1]
	v_cvt_pk_fp8_f32 v101, v109, v113 op_sel:[0,0,1]
	v_cvt_pk_fp8_f32 v102, v110, v114 op_sel:[0,0,1]
	v_cvt_pk_fp8_f32 v103, v111, v115 op_sel:[0,0,1]
	v_and_b32_e32 v104, 63, v0
	v_and_b32_e32 v106, 7, v104
	v_lshrrev_b32_e32 v104, 3, v104
	v_lshlrev_b32_e32 v104, 2, v104
	v_lshlrev_b32_e32 v105, 4, v106
	v_lshlrev_b32_e32 v106, 2, v106
	v_mad_u32_u24 v105, v106, s1, v104
	global_store_dword v105, v100, s[32:33] nt
	v_add_u32_e32 v104, s1, v105
	global_store_dword v104, v101, s[32:33] nt
	v_add_u32_e32 v106, s1, v104
	global_store_dword v106, v102, s[32:33] nt
	v_add_u32_e32 v107, s1, v106
	global_store_dword v107, v103, s[32:33] nt
.Lcn_snone_lfA:
	s_bitcmp1_b32 s26, 31
	s_cbranch_scc0 .Lcn_snone_lfB
	s_and_b32 s8, s26, 0xfffffff
	s_lshr_b32 s9, s8, 2
	s_lshl_b32 s9, s9, 11
	s_add_u32 s9, s9, s100
	s_lshr_b32 s10, s9, 9
	s_mul_i32 s10, s10, 0x2493
	s_lshr_b32 s10, s10, 16
	s_mul_i32 s11, s10, 0xe00
	s_sub_u32 s9, s9, s11
	s_and_b32 s8, s8, 3
	s_cmp_ge_u32 s10, 16
	s_cbranch_scc1 .Lcn_dn_lfBd
	s_lshr_b32 s11, s9, 5
	s_mul_i32 s11, s11, 0x2493
	s_lshr_b32 s11, s11, 16
	s_mul_i32 s12, s11, 0xe0
	s_sub_u32 s12, s9, s12
	s_lshl_b32 s11, s11, 2
	s_add_u32 s11, s11, s8
	s_lshr_b32 s9, s10, 1
	s_and_b32 s10, s10, 1
	s_mul_i32 s8, s9, 0x1c00000
	s_add_u32 s8, s8, 0x4a000000
	s_lshr_b32 s9, s12, 2
	s_lshl_b32 s9, s9, 8
	s_lshl_b32 s10, s10, 7
	s_add_u32 s9, s9, s10
	s_and_b32 s10, s12, 3
	s_lshl_b32 s10, s10, 5
	s_add_u32 s9, s9, s10
	s_lshl_b32 s9, s9, 11
	s_add_u32 s8, s8, s9
	s_lshl_b32 s9, s11, 5
	s_add_u32 s8, s8, s9
	v_readlane_b32 s32, v255, 52
	v_readlane_b32 s33, v255, 53
	s_add_u32 s32, s32, s8
	s_addc_u32 s33, s33, 0
	s_movk_i32 s1, 0x800
	s_mov_b32 s0, 0x42000000
	s_branch .Lcn_dd_lfBd

; __device__ __forceinline__ unsigned pk4_fp8(float a, float b, float c, float d) { int p = __builtin_amdgcn_cvt_pk_fp8_f32(a, b, 0, false); p = __builtin_amdgcn_cvt_pk_fp8_f32(c, d, p, true); return (unsigned)p; }
; __device__ __forceinline__ void witem_store(const WItem& w, const f32x4 (&v)[16]) {
;     if (!w.valid) return;
;     if (w.f8) {
; #pragma unroll
;         for (int j = 0; j < 4; ++j) { u32x4 o; const float sc = w.scale;
;             o.x = pk4_fp8(v[0][j] * sc, v[1][j] * sc, v[2][j] * sc, v[3][j] * sc); o.y = pk4_fp8(v[4][j] * sc, v[5][j] * sc, v[6][j] * sc, v[7][j] * sc);
;             o.z = pk4_fp8(v[8][j] * sc, v[9][j] * sc, v[10][j] * sc, v[11][j] * sc); o.w = pk4_fp8(v[12][j] * sc, v[13][j] * sc, v[14][j] * sc, v[15][j] * sc);
;             *(u32x4*)(w.dst + (size_t)witem_row(w.kind, w.n + j) * w.K + w.k0) = o; }
; __device__ __forceinline__ void p0_weights(const Args& a, LAS unsigned char* lds) {
;     ...
;         else if ((r -= I_FD) < 16 * I_MG) { const int up = r / (8 * I_MG); r -= up * 8 * I_MG; const int e = r / I_MG; r -= e * I_MG; W = a.in[up ? I_MWU : I_MWG] + (size_t)e * D * DFE; w.K = D; w.N = DFE;
;             w.dst = a.ws + WS_MGU_T + (size_t)e * 2 * DFE * D * (MOE_FP8 ? 1 : 2); w.kind = 2 + up; w.f8 = MOE_FP8; w.scale = F8_WGU; }
;         else { r -= 16 * I_MG; const int e = r / I_MD; r -= e * I_MD; W = a.in[I_MWD] + (size_t)e * DFE * D; w.K = DFE; w.N = D; w.dst = a.ws + WS_MD_T + (size_t)e * D * DFE * (MOE_FP8 ? 1 : 2); w.f8 = MOE_FP8; w.scale = F8_WD; }
;         const int nblk = (w.N + 31) >> 5, kb = r / nblk, nb = r - kb * nblk;
;         w.k0 = 128 * kb + 16 * (lane >> 3); w.n = 32 * nb + 4 * (lane & 7); w.valid = w.n < w.N; w.src = W + (size_t)w.k0 * w.N + w.n;
.Lcn_dd_lfBd:
	s_mov_b32 s26, 0
	v_mul_f32_e32 v116, s0, v116
	v_mul_f32_e32 v117, s0, v117
	v_mul_f32_e32 v118, s0, v118
	v_mul_f32_e32 v119, s0, v119
	v_mul_f32_e32 v120, s0, v120
	v_mul_f32_e32 v121, s0, v121
	v_mul_f32_e32 v122, s0, v122
	v_mul_f32_e32 v123, s0, v123
	v_mul_f32_e32 v124, s0, v124
	v_mul_f32_e32 v125, s0, v125
	v_mul_f32_e32 v126, s0, v126
	v_mul_f32_e32 v127, s0, v127
	v_mul_f32_e32 v128, s0, v128
	v_mul_f32_e32 v129, s0, v129
	v_mul_f32_e32 v130, s0, v130
	v_mul_f32_e32 v131, s0, v131
	v_cvt_pk_fp8_f32 v116, v116, v120
	v_cvt_pk_fp8_f32 v117, v117, v121
	v_cvt_pk_fp8_f32 v118, v118, v122
	v_cvt_pk_fp8_f32 v119, v119, v123
	v_cvt_pk_fp8_f32 v116, v124, v128 op_sel:[0,0,1]
	v_cvt_pk_fp8_f32 v117, v125, v129 op_sel:[0,0,1]
	v_cvt_pk_fp8_f32 v118, v126, v130 op_sel:[0,0,1]
	v_cvt_pk_fp8_f32 v119, v127, v131 op_sel:[0,0,1]
	v_and_b32_e32 v120, 63, v0
	v_and_b32_e32 v122, 7, v120
	v_lshrrev_b32_e32 v120, 3, v120
	v_lshlrev_b32_e32 v120, 2, v120
	v_lshlrev_b32_e32 v121, 4, v122
	v_lshlrev_b32_e32 v122, 2, v122
	v_mad_u32_u24 v121, v122, s1, v120
	global_store_dword v121, v116, s[32:33] nt
	v_add_u32_e32 v120, s1, v121
	global_store_dword v120, v117, s[32:33] nt
	v_add_u32_e32 v122, s1, v120
	global_store_dword v122, v118, s[32:33] nt
	v_add_u32_e32 v123, s1, v122
	global_store_dword v123, v119, s[32:33] nt
.Lcn_snone_lfB:
	s_bitcmp1_b32 s27, 31
	s_cbranch_scc0 .Lcn_snone_lfC
	s_and_b32 s8, s27, 0xfffffff
	s_lshr_b32 s9, s8, 2
	s_lshl_b32 s9, s9, 11
	s_add_u32 s9, s9, s100
	s_lshr_b32 s10, s9, 9
	s_mul_i32 s10, s10, 0x2493
	s_lshr_b32 s10, s10, 16
	s_mul_i32 s11, s10, 0xe00
	s_sub_u32 s9, s9, s11
	s_and_b32 s8, s8, 3
	s_cmp_ge_u32 s10, 16
	s_cbranch_scc1 .Lcn_dn_lfCd
	s_lshr_b32 s11, s9, 5
	s_mul_i32 s11, s11, 0x2493
	s_lshr_b32 s11, s11, 16
	s_mul_i32 s12, s11, 0xe0
	s_sub_u32 s12, s9, s12
	s_lshl_b32 s11, s11, 2
	s_add_u32 s11, s11, s8
	s_lshr_b32 s9, s10, 1
	s_and_b32 s10, s10, 1
	s_mul_i32 s8, s9, 0x1c00000
	s_add_u32 s8, s8, 0x4a000000
	s_lshr_b32 s9, s12, 2
	s_lshl_b32 s9, s9, 8
	s_lshl_b32 s10, s10, 7
	s_add_u32 s9, s9, s10
	s_and_b32 s10, s12, 3
	s_lshl_b32 s10, s10, 5
	s_add_u32 s9, s9, s10
	s_lshl_b32 s9, s9, 11
	s_add_u32 s8, s8, s9
	s_lshl_b32 s9, s11, 5
	s_add_u32 s8, s8, s9
	v_readlane_b32 s32, v255, 52
	v_readlane_b32 s33, v255, 53
	s_add_u32 s32, s32, s8
	s_addc_u32 s33, s33, 0
	s_movk_i32 s1, 0x800
	s_mov_b32 s0, 0x42000000
	s_branch .Lcn_dd_lfCd

; __device__ __forceinline__ unsigned pk4_fp8(float a, float b, float c, float d) { int p = __builtin_amdgcn_cvt_pk_fp8_f32(a, b, 0, false); p = __builtin_amdgcn_cvt_pk_fp8_f32(c, d, p, true); return (unsigned)p; }
; __device__ __forceinline__ void witem_store(const WItem& w, const f32x4 (&v)[16]) {
;     if (!w.valid) return;
;     if (w.f8) {
; #pragma unroll
;         for (int j = 0; j < 4; ++j) { u32x4 o; const float sc = w.scale;
;             o.x = pk4_fp8(v[0][j] * sc, v[1][j] * sc, v[2][j] * sc, v[3][j] * sc); o.y = pk4_fp8(v[4][j] * sc, v[5][j] * sc, v[6][j] * sc, v[7][j] * sc);
;             o.z = pk4_fp8(v[8][j] * sc, v[9][j] * sc, v[10][j] * sc, v[11][j] * sc); o.w = pk4_fp8(v[12][j] * sc, v[13][j] * sc, v[14][j] * sc, v[15][j] * sc);
;             *(u32x4*)(w.dst + (size_t)witem_row(w.kind, w.n + j) * w.K + w.k0) = o; }
; __device__ __forceinline__ void p0_weights(const Args& a, LAS unsigned char* lds) {
;     ...
;         else if ((r -= I_FD) < 16 * I_MG) { const int up = r / (8 * I_MG); r -= up * 8 * I_MG; const int e = r / I_MG; r -= e * I_MG; W = a.in[up ? I_MWU : I_MWG] + (size_t)e * D * DFE; w.K = D; w.N = DFE;
;             w.dst = a.ws + WS_MGU_T + (size_t)e * 2 * DFE * D * (MOE_FP8 ? 1 : 2); w.kind = 2 + up; w.f8 = MOE_FP8; w.scale = F8_WGU; }
;         else { r -= 16 * I_MG; const int e = r / I_MD; r -= e * I_MD; W = a.in[I_MWD] + (size_t)e * DFE * D; w.K = DFE; w.N = D; w.dst = a.ws + WS_MD_T + (size_t)e * D * DFE * (MOE_FP8 ? 1 : 2); w.f8 = MOE_FP8; w.scale = F8_WD; }
;         const int nblk = (w.N + 31) >> 5, kb = r / nblk, nb = r - kb * nblk;
;         w.k0 = 128 * kb + 16 * (lane >> 3); w.n = 32 * nb + 4 * (lane & 7); w.valid = w.n < w.N; w.src = W + (size_t)w.k0 * w.N + w.n;
.Lcn_dd_lfCd:
	s_mov_b32 s27, 0
	v_mul_f32_e32 v132, s0, v132
	v_mul_f32_e32 v133, s0, v133
	v_mul_f32_e32 v134, s0, v134
	v_mul_f32_e32 v135, s0, v135
	v_mul_f32_e32 v136, s0, v136
	v_mul_f32_e32 v137, s0, v137
	v_mul_f32_e32 v138, s0, v138
	v_mul_f32_e32 v139, s0, v139
	v_mul_f32_e32 v140, s0, v140
	v_mul_f32_e32 v141, s0, v141
	v_mul_f32_e32 v142, s0, v142
	v_mul_f32_e32 v143, s0, v143
	v_mul_f32_e32 v144, s0, v144
	v_mul_f32_e32 v145, s0, v145
	v_mul_f32_e32 v146, s0, v146
	v_mul_f32_e32 v147, s0, v147
	v_cvt_pk_fp8_f32 v132, v132, v136
	v_cvt_pk_fp8_f32 v133, v133, v137
	v_cvt_pk_fp8_f32 v134, v134, v138
	v_cvt_pk_fp8_f32 v135, v135, v139
	v_cvt_pk_fp8_f32 v132, v140, v144 op_sel:[0,0,1]
	v_cvt_pk_fp8_f32 v133, v141, v145 op_sel:[0,0,1]
	v_cvt_pk_fp8_f32 v134, v142, v146 op_sel:[0,0,1]
	v_cvt_pk_fp8_f32 v135, v143, v147 op_sel:[0,0,1]
	v_and_b32_e32 v136, 63, v0
	v_and_b32_e32 v138, 7, v136
	v_lshrrev_b32_e32 v136, 3, v136
	v_lshlrev_b32_e32 v136, 2, v136
	v_lshlrev_b32_e32 v137, 4, v138
	v_lshlrev_b32_e32 v138, 2, v138
	v_mad_u32_u24 v137, v138, s1, v136
	global_store_dword v137, v132, s[32:33] nt
	v_add_u32_e32 v136, s1, v137
	global_store_dword v136, v133, s[32:33] nt
	v_add_u32_e32 v138, s1, v136
	global_store_dword v138, v134, s[32:33] nt
	v_add_u32_e32 v139, s1, v138
	global_store_dword v139, v135, s[32:33] nt
.Lcn_snone_lfC:
	s_bitcmp1_b32 s28, 31
	s_cbranch_scc0 .Lcn_snone_lfD
	s_and_b32 s8, s28, 0xfffffff
	s_lshr_b32 s9, s8, 2
	s_lshl_b32 s9, s9, 11
	s_add_u32 s9, s9, s100
	s_lshr_b32 s10, s9, 9
	s_mul_i32 s10, s10, 0x2493
	s_lshr_b32 s10, s10, 16
	s_mul_i32 s11, s10, 0xe00
	s_sub_u32 s9, s9, s11
	s_and_b32 s8, s8, 3
	s_cmp_ge_u32 s10, 16
	s_cbranch_scc1 .Lcn_dn_lfDd
	s_lshr_b32 s11, s9, 5
	s_mul_i32 s11, s11, 0x2493
	s_lshr_b32 s11, s11, 16
	s_mul_i32 s12, s11, 0xe0
	s_sub_u32 s12, s9, s12
	s_lshl_b32 s11, s11, 2
	s_add_u32 s11, s11, s8
	s_lshr_b32 s9, s10, 1
	s_and_b32 s10, s10, 1
	s_mul_i32 s8, s9, 0x1c00000
	s_add_u32 s8, s8, 0x4a000000
	s_lshr_b32 s9, s12, 2
	s_lshl_b32 s9, s9, 8
	s_lshl_b32 s10, s10, 7
	s_add_u32 s9, s9, s10
	s_and_b32 s10, s12, 3
	s_lshl_b32 s10, s10, 5
	s_add_u32 s9, s9, s10
	s_lshl_b32 s9, s9, 11
	s_add_u32 s8, s8, s9
	s_lshl_b32 s9, s11, 5
	s_add_u32 s8, s8, s9
	v_readlane_b32 s32, v255, 52
	v_readlane_b32 s33, v255, 53
	s_add_u32 s32, s32, s8
	s_addc_u32 s33, s33, 0
	s_movk_i32 s1, 0x800
	s_mov_b32 s0, 0x42000000
	s_branch .Lcn_dd_lfDd

; __device__ __forceinline__ unsigned pk4_fp8(float a, float b, float c, float d) { int p = __builtin_amdgcn_cvt_pk_fp8_f32(a, b, 0, false); p = __builtin_amdgcn_cvt_pk_fp8_f32(c, d, p, true); return (unsigned)p; }
; __device__ __forceinline__ void witem_store(const WItem& w, const f32x4 (&v)[16]) {
;     if (!w.valid) return;
;     if (w.f8) {
; #pragma unroll
;         for (int j = 0; j < 4; ++j) { u32x4 o; const float sc = w.scale;
;             o.x = pk4_fp8(v[0][j] * sc, v[1][j] * sc, v[2][j] * sc, v[3][j] * sc); o.y = pk4_fp8(v[4][j] * sc, v[5][j] * sc, v[6][j] * sc, v[7][j] * sc);
;             o.z = pk4_fp8(v[8][j] * sc, v[9][j] * sc, v[10][j] * sc, v[11][j] * sc); o.w = pk4_fp8(v[12][j] * sc, v[13][j] * sc, v[14][j] * sc, v[15][j] * sc);
;             *(u32x4*)(w.dst + (size_t)witem_row(w.kind, w.n + j) * w.K + w.k0) = o; }
.Lcn_dd_lfDd:
	s_mov_b32 s28, 0
	v_mul_f32_e32 v148, s0, v148
	v_mul_f32_e32 v149, s0, v149
	v_mul_f32_e32 v150, s0, v150
	v_mul_f32_e32 v151, s0, v151
	v_mul_f32_e32 v152, s0, v152
	v_mul_f32_e32 v153, s0, v153
	v_mul_f32_e32 v154, s0, v154
	v_mul_f32_e32 v155, s0, v155
	v_mul_f32_e32 v156, s0, v156
	v_mul_f32_e32 v157, s0, v157
	v_mul_f32_e32 v158, s0, v158
	v_mul_f32_e32 v159, s0, v159
	v_mul_f32_e32 v160, s0, v160
	v_mul_f32_e32 v161, s0, v161
	v_mul_f32_e32 v162, s0, v162
	v_mul_f32_e32 v163, s0, v163
	v_cvt_pk_fp8_f32 v148, v148, v152
	v_cvt_pk_fp8_f32 v149, v149, v153
	v_cvt_pk_fp8_f32 v150, v150, v154
	v_cvt_pk_fp8_f32 v151, v151, v155
	v_cvt_pk_fp8_f32 v148, v156, v160 op_sel:[0,0,1]
	v_cvt_pk_fp8_f32 v149, v157, v161 op_sel:[0,0,1]
	v_cvt_pk_fp8_f32 v150, v158, v162 op_sel:[0,0,1]
	v_cvt_pk_fp8_f32 v151, v159, v163 op_sel:[0,0,1]
	v_and_b32_e32 v152, 63, v0
	v_and_b32_e32 v154, 7, v152
	v_lshrrev_b32_e32 v152, 3, v152
	v_lshlrev_b32_e32 v152, 2, v152
	v_lshlrev_b32_e32 v153, 4, v154
	v_lshlrev_b32_e32 v154, 2, v154
	v_mad_u32_u24 v153, v154, s1, v152
	global_store_dword v153, v148, s[32:33] nt
	v_add_u32_e32 v152, s1, v153
	global_store_dword v152, v149, s[32:33] nt
	v_add_u32_e32 v154, s1, v152
	global_store_dword v154, v150, s[32:33] nt
	v_add_u32_e32 v155, s1, v154
	global_store_dword v155, v151, s[32:33] nt
